# P10: sort trimmed (last merge's in-block stages skipped); V-side nibble mask 0xf000f0 moved from a 32-bit literal into s32
# baseline (speedup 1.0000x reference)
; #define EXP_XROW(tt) do { const char* g_ = (const char*)(xin + (size_t)(tt) * 1024) + lane * 16; LAS unsigned char* l_ = xslot + ((tt) & 1) * 2048; \
;         __builtin_amdgcn_global_load_lds((const unsigned*)g_, (LAS unsigned*)l_, 16, 0, 2); __builtin_amdgcn_global_load_lds((const unsigned*)(g_ + 1024), (LAS unsigned*)(l_ + 1024), 16, 0, 2); } while (0)
; __device__ __forceinline__ void expert_tokens(const unsigned char* __restrict__ UV, const float* __restrict__ US, const float* __restrict__ VS, ...
;     if (t0 >= t1) return;
;     const unsigned lo16 = (unsigned)lane * 16u;
;     const int el = ((lane >> 5) & 1) * 8 + ((lane >> 4) & 1) * 4 + ((lane >> 1) & 1) * 2 + (lane & 1);
;     const unsigned cw0 = (unsigned)IDX[(size_t)t0 * 128 + lane], cw1 = (unsigned)IDX[(size_t)t0 * 128 + 64 + lane];
;     int ci0 = (int)cw0 & rmask, ci1 = (int)cw1 & rmask;
;     float cg0 = __uint_as_float(cw0 & 0xFFFF0000u), cg1 = __uint_as_float(cw1 & 0xFFFF0000u);
;     float csu0 = US[ci0], csu1 = US[ci1], csv0 = VS[ci0], csv1 = VS[ci1];
;     ...
;     EXP_XROW(t0);
; __global__ void __launch_bounds__(NTHREADS, 2) mega(Args a) {
;     ...
;                 const int t0 = gw * tpw, t1 = (t0 + tpw < T) ? t0 + tpw : T;
;                 if (rep_ == 0 && DUP_MODE == 2) { for (int t = t0; t < t1; ++t) gather_only_token((const unsigned char*)(ws + WS_UQ), IDX, outp, t, lane); } else
;                 expert_tokens((const unsigned char*)(ws + WS_UQ), (const float*)(ws + WS_US), (const float*)(ws + WS_VS), IDX, GATE, pv, (const bf16_t*)(ws + WS_HST), lds + 16384 + wave * 4096, outp, t0, t1, lane, rmask, pd);
.LBB0_1011:
	s_or_b64 exec, exec, s[12:13]
	s_waitcnt lgkmcnt(0)
	s_mul_i32 s8, s24, s96
	s_add_i32 s0, s8, s24
	s_min_i32 s17, s0, 0x8000
	s_sub_i32 s77, s96, s95
	s_add_i32 s77, s77, 8
	s_mul_i32 s77, s77, s24
	s_cmp_le_i32 s77, 0x8000
	s_cselect_b32 s77, 1, 0
	s_cmp_ge_i32 s8, s17
	s_waitcnt vmcnt(0)
	s_barrier
	s_cbranch_scc1 .LBB0_1025
	s_add_u32 s0, s6, 0xf800000
	s_addc_u32 s1, s7, 0
	s_add_u32 s10, s6, 0x1200000
	s_addc_u32 s11, s7, 0
	s_mov_b32 s80, s10
	s_and_b32 s81, s11, 0xffff
	s_mov_b32 s82, 0x1000000
	s_mov_b32 s83, 0x20000
	s_mov_b32 s32, 0xf000f0
	s_add_u32 s12, s6, 0x1100000
	s_addc_u32 s13, s7, 0
	s_add_u32 s14, s6, 0x1140000
	s_addc_u32 s15, s7, 0
	s_lshl_b32 s2, s95, 12
	s_add_i32 s26, s2, 0
	s_add_u32 s2, s6, 0x1b800000
	s_addc_u32 s3, s7, 0
	s_ashr_i32 s9, s8, 31
	s_lshl_b64 s[6:7], s[8:9], 9
	v_and_b32_e32 v74, 63, v0
	s_add_u32 s6, s0, s6
	s_addc_u32 s7, s1, s7
	v_lshlrev_b32_e32 v192, 2, v74
	global_load_dword v229, v192, s[6:7]
	global_load_dword v230, v192, s[6:7] offset:256
	s_lshl_b64 s[18:19], s[8:9], 11
	s_add_u32 s18, s2, s18
	s_addc_u32 s19, s3, s19
	s_lshl_b32 s9, s8, 11
	v_mov_b32_e32 v1, 0
	s_and_b32 s9, s9, 0x800
	v_lshlrev_b32_e32 v194, 4, v74
	v_mov_b32_e32 v195, v1
	s_add_i32 s9, s26, s9
	s_mov_b64 s[6:7], 0x400
	v_lshl_add_u64 v[2:3], s[18:19], 0, v[194:195]
	s_add_i32 m0, s9, 0x4000
	v_lshl_add_u64 v[2:3], v[2:3], 0, s[6:7]
	global_load_lds_dwordx4 v194, s[18:19] nt
	s_add_i32 m0, s9, 0x4400
	v_mov_b32_e32 v193, v1
	global_load_lds_dwordx4 v[2:3], off nt
	v_and_b32_e32 v77, 2, v0
	v_lshl_add_u64 v[196:197], s[0:1], 0, v[192:193]
	v_lshl_add_u64 v[198:199], s[2:3], 0, v[194:195]
	v_cmp_eq_u32_e64 s[0:1], 0, v77
	v_lshl_add_u64 v[200:201], s[4:5], 0, v[194:195]
	v_lshl_add_u32 v195, v74, 3, s26
	v_mov_b32_e32 v226, 0x358637bd
	v_mov_b32_e32 v227, 0xbf3a00e3
	s_waitcnt vmcnt(0)
	v_alignbit_b32 v229, v229, v229, 16
	v_alignbit_b32 v230, v230, v230, 16
	s_nop 1
	s_mov_b32 s58, 0x99999999
	s_mov_b32 s59, 0x99999999
	v_min_u32_dpp v202, v229, v229 quad_perm:[1,0,3,2] row_mask:0xf bank_mask:0xf
	v_max_u32_dpp v203, v229, v229 quad_perm:[1,0,3,2] row_mask:0xf bank_mask:0xf
	v_min_u32_dpp v204, v230, v230 quad_perm:[1,0,3,2] row_mask:0xf bank_mask:0xf
	v_max_u32_dpp v205, v230, v230 quad_perm:[1,0,3,2] row_mask:0xf bank_mask:0xf
	v_cndmask_b32_e64 v229, v203, v202, s[58:59]
	v_cndmask_b32_e64 v230, v205, v204, s[58:59]
	s_mov_b32 s58, 0xcc33cc33
	s_mov_b32 s59, 0xcc33cc33
	v_min_u32_dpp v202, v229, v229 quad_perm:[2,3,0,1] row_mask:0xf bank_mask:0xf
	v_max_u32_dpp v203, v229, v229 quad_perm:[2,3,0,1] row_mask:0xf bank_mask:0xf
	v_min_u32_dpp v204, v230, v230 quad_perm:[2,3,0,1] row_mask:0xf bank_mask:0xf
	v_max_u32_dpp v205, v230, v230 quad_perm:[2,3,0,1] row_mask:0xf bank_mask:0xf
	v_cndmask_b32_e64 v229, v203, v202, s[58:59]
	v_cndmask_b32_e64 v230, v205, v204, s[58:59]
	s_mov_b32 s58, 0xaa55aa55
	s_mov_b32 s59, 0xaa55aa55
	v_min_u32_dpp v202, v229, v229 quad_perm:[1,0,3,2] row_mask:0xf bank_mask:0xf
	v_max_u32_dpp v203, v229, v229 quad_perm:[1,0,3,2] row_mask:0xf bank_mask:0xf
	v_min_u32_dpp v204, v230, v230 quad_perm:[1,0,3,2] row_mask:0xf bank_mask:0xf
	v_max_u32_dpp v205, v230, v230 quad_perm:[1,0,3,2] row_mask:0xf bank_mask:0xf
	v_cndmask_b32_e64 v229, v203, v202, s[58:59]
	v_cndmask_b32_e64 v230, v205, v204, s[58:59]
	s_mov_b32 s58, 0xf00ff00f
	s_mov_b32 s59, 0xf00ff00f
	v_min_u32_dpp v202, v229, v229 row_ror:8 row_mask:0xf bank_mask:0xf
	v_max_u32_dpp v203, v229, v229 row_ror:8 row_mask:0xf bank_mask:0xf
	v_min_u32_dpp v204, v230, v230 row_ror:8 row_mask:0xf bank_mask:0xf
	v_max_u32_dpp v205, v230, v230 row_ror:8 row_mask:0xf bank_mask:0xf
	v_cndmask_b32_e64 v229, v203, v202, s[58:59]
	v_cndmask_b32_e64 v230, v205, v204, s[58:59]
	s_mov_b32 s58, 0xc3c3c3c3
	s_mov_b32 s59, 0xc3c3c3c3
	v_min_u32_dpp v202, v229, v229 quad_perm:[2,3,0,1] row_mask:0xf bank_mask:0xf
	v_max_u32_dpp v203, v229, v229 quad_perm:[2,3,0,1] row_mask:0xf bank_mask:0xf
	v_min_u32_dpp v204, v230, v230 quad_perm:[2,3,0,1] row_mask:0xf bank_mask:0xf
	v_max_u32_dpp v205, v230, v230 quad_perm:[2,3,0,1] row_mask:0xf bank_mask:0xf
	v_cndmask_b32_e64 v229, v203, v202, s[58:59]
	v_cndmask_b32_e64 v230, v205, v204, s[58:59]
	s_mov_b32 s58, 0xa5a5a5a5
	s_mov_b32 s59, 0xa5a5a5a5
	v_min_u32_dpp v202, v229, v229 quad_perm:[1,0,3,2] row_mask:0xf bank_mask:0xf
	v_max_u32_dpp v203, v229, v229 quad_perm:[1,0,3,2] row_mask:0xf bank_mask:0xf
	v_min_u32_dpp v204, v230, v230 quad_perm:[1,0,3,2] row_mask:0xf bank_mask:0xf
	v_max_u32_dpp v205, v230, v230 quad_perm:[1,0,3,2] row_mask:0xf bank_mask:0xf
	v_cndmask_b32_e64 v229, v203, v202, s[58:59]
	v_cndmask_b32_e64 v230, v205, v204, s[58:59]
	s_mov_b32 s58, 0xf0f00f0f
	s_mov_b32 s59, 0xf0f00f0f
	v_mov_b32_dpp v202, v229 row_half_mirror row_mask:0xf bank_mask:0xf
	v_mov_b32_dpp v204, v230 row_half_mirror row_mask:0xf bank_mask:0xf
	s_nop 0
	v_max_u32_dpp v203, v202, v229 quad_perm:[3,2,1,0] row_mask:0xf bank_mask:0xf
	v_max_u32_dpp v205, v204, v230 quad_perm:[3,2,1,0] row_mask:0xf bank_mask:0xf
	v_min_u32_dpp v202, v202, v229 quad_perm:[3,2,1,0] row_mask:0xf bank_mask:0xf
	v_min_u32_dpp v204, v204, v230 quad_perm:[3,2,1,0] row_mask:0xf bank_mask:0xf
	v_cndmask_b32_e64 v229, v203, v202, s[58:59]
	v_cndmask_b32_e64 v230, v205, v204, s[58:59]
	s_mov_b32 s58, 0xff0000ff
	s_mov_b32 s59, 0xff0000ff
	v_min_u32_dpp v202, v229, v229 row_ror:8 row_mask:0xf bank_mask:0xf
	v_max_u32_dpp v203, v229, v229 row_ror:8 row_mask:0xf bank_mask:0xf
	v_min_u32_dpp v204, v230, v230 row_ror:8 row_mask:0xf bank_mask:0xf
	v_max_u32_dpp v205, v230, v230 row_ror:8 row_mask:0xf bank_mask:0xf
	v_cndmask_b32_e64 v229, v203, v202, s[58:59]
; __device__ __forceinline__ void expert_tokens(const unsigned char* __restrict__ UV, const float* __restrict__ US, const float* __restrict__ VS, ...
;     ...
;     const unsigned cw0 = (unsigned)IDX[(size_t)t0 * 128 + lane], cw1 = (unsigned)IDX[(size_t)t0 * 128 + 64 + lane];
;     int ci0 = (int)cw0 & rmask, ci1 = (int)cw1 & rmask;
	v_cndmask_b32_e64 v230, v205, v204, s[58:59]
	s_mov_b32 s58, 0xcccc3333
	s_mov_b32 s59, 0xcccc3333
	v_min_u32_dpp v202, v229, v229 quad_perm:[2,3,0,1] row_mask:0xf bank_mask:0xf
	v_max_u32_dpp v203, v229, v229 quad_perm:[2,3,0,1] row_mask:0xf bank_mask:0xf
	v_min_u32_dpp v204, v230, v230 quad_perm:[2,3,0,1] row_mask:0xf bank_mask:0xf
	v_max_u32_dpp v205, v230, v230 quad_perm:[2,3,0,1] row_mask:0xf bank_mask:0xf
	v_cndmask_b32_e64 v229, v203, v202, s[58:59]
	v_cndmask_b32_e64 v230, v205, v204, s[58:59]
	s_mov_b32 s58, 0xaaaa5555
	s_mov_b32 s59, 0xaaaa5555
	v_min_u32_dpp v202, v229, v229 quad_perm:[1,0,3,2] row_mask:0xf bank_mask:0xf
	v_max_u32_dpp v203, v229, v229 quad_perm:[1,0,3,2] row_mask:0xf bank_mask:0xf
	v_min_u32_dpp v204, v230, v230 quad_perm:[1,0,3,2] row_mask:0xf bank_mask:0xf
	v_max_u32_dpp v205, v230, v230 quad_perm:[1,0,3,2] row_mask:0xf bank_mask:0xf
	v_cndmask_b32_e64 v229, v203, v202, s[58:59]
	v_cndmask_b32_e64 v230, v205, v204, s[58:59]
	s_nop 1
	v_permlane16_swap_b32_e32 v229, v230
	s_mov_b32 s58, -1
	s_mov_b32 s59, 0
	v_min_u32_e32 v202, v229, v230
	v_max_u32_e32 v203, v229, v230
	v_cndmask_b32_e64 v229, v203, v202, s[58:59]
	v_cndmask_b32_e64 v230, v202, v203, s[58:59]
	s_mov_b32 s58, 0xf0f0f0f
	s_mov_b32 s59, 0xf0f0f0f0
	v_mov_b32_dpp v202, v229 row_half_mirror row_mask:0xf bank_mask:0xf
	v_mov_b32_dpp v204, v230 row_half_mirror row_mask:0xf bank_mask:0xf
	s_nop 0
	v_max_u32_dpp v203, v202, v229 quad_perm:[3,2,1,0] row_mask:0xf bank_mask:0xf
	v_max_u32_dpp v205, v204, v230 quad_perm:[3,2,1,0] row_mask:0xf bank_mask:0xf
	v_min_u32_dpp v202, v202, v229 quad_perm:[3,2,1,0] row_mask:0xf bank_mask:0xf
	v_min_u32_dpp v204, v204, v230 quad_perm:[3,2,1,0] row_mask:0xf bank_mask:0xf
	v_cndmask_b32_e64 v229, v203, v202, s[58:59]
	v_cndmask_b32_e64 v230, v205, v204, s[58:59]
	s_mov_b32 s58, 0xff00ff
	s_mov_b32 s59, 0xff00ff00
	v_min_u32_dpp v202, v229, v229 row_ror:8 row_mask:0xf bank_mask:0xf
	v_max_u32_dpp v203, v229, v229 row_ror:8 row_mask:0xf bank_mask:0xf
	v_min_u32_dpp v204, v230, v230 row_ror:8 row_mask:0xf bank_mask:0xf
	v_max_u32_dpp v205, v230, v230 row_ror:8 row_mask:0xf bank_mask:0xf
	v_cndmask_b32_e64 v229, v203, v202, s[58:59]
	v_cndmask_b32_e64 v230, v205, v204, s[58:59]
	s_mov_b32 s58, 0x33333333
	s_mov_b32 s59, 0xcccccccc
	v_min_u32_dpp v202, v229, v229 quad_perm:[2,3,0,1] row_mask:0xf bank_mask:0xf
	v_max_u32_dpp v203, v229, v229 quad_perm:[2,3,0,1] row_mask:0xf bank_mask:0xf
	v_min_u32_dpp v204, v230, v230 quad_perm:[2,3,0,1] row_mask:0xf bank_mask:0xf
	v_max_u32_dpp v205, v230, v230 quad_perm:[2,3,0,1] row_mask:0xf bank_mask:0xf
	v_cndmask_b32_e64 v229, v203, v202, s[58:59]
	v_cndmask_b32_e64 v230, v205, v204, s[58:59]
	s_mov_b32 s58, 0x55555555
	s_mov_b32 s59, 0xaaaaaaaa
	v_min_u32_dpp v202, v229, v229 quad_perm:[1,0,3,2] row_mask:0xf bank_mask:0xf
	v_max_u32_dpp v203, v229, v229 quad_perm:[1,0,3,2] row_mask:0xf bank_mask:0xf
	v_min_u32_dpp v204, v230, v230 quad_perm:[1,0,3,2] row_mask:0xf bank_mask:0xf
	v_max_u32_dpp v205, v230, v230 quad_perm:[1,0,3,2] row_mask:0xf bank_mask:0xf
	v_cndmask_b32_e64 v229, v203, v202, s[58:59]
	v_cndmask_b32_e64 v230, v205, v204, s[58:59]
	s_nop 1
	v_permlane32_swap_b32_e32 v229, v230
	s_mov_b32 s58, 0xffff
	s_mov_b32 s59, 0xffff
	v_min_u32_e32 v202, v229, v230
	v_max_u32_e32 v203, v229, v230
	v_cndmask_b32_e64 v229, v203, v202, s[58:59]
	v_cndmask_b32_e64 v230, v202, v203, s[58:59]
	s_nop 1
	v_permlane32_swap_b32_e32 v229, v230
	s_mov_b32 s58, 0xffff
	s_mov_b32 s59, 0xffff
	v_min_u32_e32 v202, v229, v230
	v_max_u32_e32 v203, v229, v230
	v_cndmask_b32_e64 v229, v203, v202, s[58:59]
	v_cndmask_b32_e64 v230, v202, v203, s[58:59]
	s_mov_b32 s58, 0xf0f00f0f
	s_mov_b32 s59, 0xf0f00f0f
	v_mov_b32_dpp v202, v229 row_half_mirror row_mask:0xf bank_mask:0xf
	v_mov_b32_dpp v204, v230 row_half_mirror row_mask:0xf bank_mask:0xf
	s_nop 0
	v_max_u32_dpp v203, v202, v229 quad_perm:[3,2,1,0] row_mask:0xf bank_mask:0xf
	v_max_u32_dpp v205, v204, v230 quad_perm:[3,2,1,0] row_mask:0xf bank_mask:0xf
	v_min_u32_dpp v202, v202, v229 quad_perm:[3,2,1,0] row_mask:0xf bank_mask:0xf
	v_min_u32_dpp v204, v204, v230 quad_perm:[3,2,1,0] row_mask:0xf bank_mask:0xf
	v_cndmask_b32_e64 v229, v203, v202, s[58:59]
	v_cndmask_b32_e64 v230, v205, v204, s[58:59]
	s_mov_b32 s58, 0xff0000ff
	s_mov_b32 s59, 0xff0000ff
	v_min_u32_dpp v202, v229, v229 row_ror:8 row_mask:0xf bank_mask:0xf
	v_max_u32_dpp v203, v229, v229 row_ror:8 row_mask:0xf bank_mask:0xf
	v_min_u32_dpp v204, v230, v230 row_ror:8 row_mask:0xf bank_mask:0xf
	v_max_u32_dpp v205, v230, v230 row_ror:8 row_mask:0xf bank_mask:0xf
	v_cndmask_b32_e64 v229, v203, v202, s[58:59]
	v_cndmask_b32_e64 v230, v205, v204, s[58:59]
	s_mov_b32 s58, 0xcccc3333
	s_mov_b32 s59, 0xcccc3333
	v_min_u32_dpp v202, v229, v229 quad_perm:[2,3,0,1] row_mask:0xf bank_mask:0xf
	v_max_u32_dpp v203, v229, v229 quad_perm:[2,3,0,1] row_mask:0xf bank_mask:0xf
	v_min_u32_dpp v204, v230, v230 quad_perm:[2,3,0,1] row_mask:0xf bank_mask:0xf
	v_max_u32_dpp v205, v230, v230 quad_perm:[2,3,0,1] row_mask:0xf bank_mask:0xf
	v_cndmask_b32_e64 v229, v203, v202, s[58:59]
	v_cndmask_b32_e64 v230, v205, v204, s[58:59]
	s_mov_b32 s58, 0xaaaa5555
	s_mov_b32 s59, 0xaaaa5555
; #define EXP_ROW(src, l) (*(const u32x4*)(UV + ((unsigned)__builtin_amdgcn_readlane((src), (l)) * 1024u + lo16)))
; #define EXP_XROW(tt) do { const char* g_ = (const char*)(xin + (size_t)(tt) * 1024) + lane * 16; LAS unsigned char* l_ = xslot + ((tt) & 1) * 2048; \
;         __builtin_amdgcn_global_load_lds((const unsigned*)g_, (LAS unsigned*)l_, 16, 0, 2); __builtin_amdgcn_global_load_lds((const unsigned*)(g_ + 1024), (LAS unsigned*)(l_ + 1024), 16, 0, 2); } while (0)
; __device__ __forceinline__ void expert_tokens(const unsigned char* __restrict__ UV, const float* __restrict__ US, const float* __restrict__ VS, ...
;     ...
;     int ci0 = (int)cw0 & rmask, ci1 = (int)cw1 & rmask;
;     float cg0 = __uint_as_float(cw0 & 0xFFFF0000u), cg1 = __uint_as_float(cw1 & 0xFFFF0000u);
;     float csu0 = US[ci0], csu1 = US[ci1], csv0 = VS[ci0], csv1 = VS[ci1];
;     ...
;     EXP_XROW(t0);
;     u32x4 A[EB], B[EB];
; #pragma unroll
;     for (int e = 0; e < EB; ++e) A[e] = EXP_ROW(ci0, e);
; #pragma unroll
;     for (int e = 0; e < EB; ++e) B[e] = EXP_ROW(ci0, EB + e);
	v_min_u32_dpp v202, v229, v229 quad_perm:[1,0,3,2] row_mask:0xf bank_mask:0xf
	v_max_u32_dpp v203, v229, v229 quad_perm:[1,0,3,2] row_mask:0xf bank_mask:0xf
	v_min_u32_dpp v204, v230, v230 quad_perm:[1,0,3,2] row_mask:0xf bank_mask:0xf
	v_max_u32_dpp v205, v230, v230 quad_perm:[1,0,3,2] row_mask:0xf bank_mask:0xf
	v_cndmask_b32_e64 v229, v203, v202, s[58:59]
	v_cndmask_b32_e64 v230, v205, v204, s[58:59]
	s_nop 1
	v_permlane16_swap_b32_e32 v229, v230
	v_min_u32_e32 v202, v229, v230
	v_max_u32_e32 v230, v229, v230
	v_mov_b32_e32 v229, v202
	s_nop 1
	v_permlane32_swap_b32_e32 v229, v230
	v_min_u32_e32 v202, v229, v230
	v_max_u32_e32 v230, v229, v230
	v_mov_b32_e32 v229, v202
	s_nop 1
	v_permlane16_swap_b32_e32 v229, v230
	v_min_u32_e32 v202, v229, v230
	v_max_u32_e32 v230, v229, v230
	v_mov_b32_e32 v229, v202
	s_nop 1
	v_permlane16_swap_b32_e32 v229, v230
	s_nop 1
	v_permlane32_swap_b32_e32 v229, v230
	v_alignbit_b32 v229, v229, v229, 16
	v_alignbit_b32 v230, v230, v230, 16
	v_and_b32_e32 v231, 0x3fff, v229
	v_and_b32_e32 v232, 0x3fff, v230
	v_readlane_b32 s40, v231, 22
	v_readlane_b32 s41, v231, 23
	v_readlane_b32 s49, v231, 31
	v_lshlrev_b32_e32 v2, 2, v231
	v_lshlrev_b32_e32 v3, 2, v232
	v_readlane_b32 s33, v231, 15
	v_readlane_b32 s34, v231, 16
	v_readlane_b32 s35, v231, 17
	v_readlane_b32 s36, v231, 18
	v_readlane_b32 s37, v231, 19
	v_readlane_b32 s38, v231, 20
	v_readlane_b32 s39, v231, 21
	v_readlane_b32 s42, v231, 24
	v_readlane_b32 s43, v231, 25
	v_readlane_b32 s44, v231, 26
	v_readlane_b32 s45, v231, 27
	v_readlane_b32 s46, v231, 28
	v_readlane_b32 s47, v231, 29
	v_readlane_b32 s48, v231, 30
	v_lshl_or_b32 v42, s49, 10, v194
	v_lshl_or_b32 v50, s41, 10, v194
	v_lshl_or_b32 v51, s40, 10, v194
	v_readlane_b32 s30, v231, 13
	v_readlane_b32 s31, v231, 14
	global_load_dword v233, v2, s[12:13]
	global_load_dword v234, v3, s[12:13]
	global_load_dword v236, v3, s[14:15]
	global_load_dword v235, v2, s[14:15]
	v_lshl_or_b32 v43, s48, 10, v194
	v_lshl_or_b32 v44, s47, 10, v194
	v_lshl_or_b32 v45, s46, 10, v194
	v_lshl_or_b32 v46, s45, 10, v194
	v_lshl_or_b32 v47, s44, 10, v194
	v_lshl_or_b32 v48, s43, 10, v194
	v_lshl_or_b32 v49, s42, 10, v194
	global_load_dwordx4 v[2:5], v42, s[10:11]
	global_load_dwordx4 v[10:13], v43, s[10:11]
	global_load_dwordx4 v[6:9], v44, s[10:11]
	global_load_dwordx4 v[18:21], v45, s[10:11]
	global_load_dwordx4 v[14:17], v46, s[10:11]
	global_load_dwordx4 v[26:29], v47, s[10:11]
	global_load_dwordx4 v[22:25], v48, s[10:11]
	global_load_dwordx4 v[34:37], v49, s[10:11]
	global_load_dwordx4 v[30:33], v50, s[10:11]
	global_load_dwordx4 v[38:41], v51, s[10:11]
	v_lshl_or_b32 v50, s39, 10, v194
	v_lshl_or_b32 v51, s38, 10, v194
	v_lshl_or_b32 v58, s37, 10, v194
	v_lshl_or_b32 v59, s36, 10, v194
	v_lshl_or_b32 v66, s35, 10, v194
	v_lshl_or_b32 v67, s34, 10, v194
	v_lshl_or_b32 v75, s33, 10, v194
	v_readlane_b32 s28, v231, 11
	v_readlane_b32 s29, v231, 12
	global_load_dwordx4 v[42:45], v50, s[10:11]
	global_load_dwordx4 v[46:49], v51, s[10:11]
	s_nop 0
	global_load_dwordx4 v[50:53], v58, s[10:11]
	global_load_dwordx4 v[54:57], v59, s[10:11]
	s_nop 0
	global_load_dwordx4 v[58:61], v66, s[10:11]
	global_load_dwordx4 v[62:65], v67, s[10:11]
	v_lshl_or_b32 v76, s31, 10, v194
	global_load_dwordx4 v[66:69], v75, s[10:11]
	global_load_dwordx4 v[70:73], v76, s[10:11]
	v_lshl_or_b32 v75, s30, 10, v194
	v_readlane_b32 s25, v231, 9
	v_readlane_b32 s27, v231, 10
	v_lshl_or_b32 v76, s29, 10, v194
	global_load_dwordx4 v[112:115], v75, s[10:11]
	global_load_dwordx4 v[116:119], v76, s[10:11]
	v_lshl_or_b32 v75, s28, 10, v194
	v_readlane_b32 s23, v231, 7
	v_readlane_b32 s24, v231, 8
	v_lshl_or_b32 v76, s27, 10, v194
	global_load_dwordx4 v[144:147], v75, s[10:11]
	global_load_dwordx4 v[148:151], v76, s[10:11]
	v_lshl_or_b32 v75, s25, 10, v194
	v_readlane_b32 s21, v231, 5
	v_readlane_b32 s22, v231, 6
	v_lshl_or_b32 v76, s24, 10, v194
	global_load_dwordx4 v[152:155], v75, s[10:11]
	global_load_dwordx4 v[156:159], v76, s[10:11]
	v_lshl_or_b32 v75, s23, 10, v194
	v_readlane_b32 s19, v231, 3
	v_readlane_b32 s20, v231, 4
	v_lshl_or_b32 v76, s22, 10, v194
	global_load_dwordx4 v[160:163], v75, s[10:11]
	global_load_dwordx4 v[164:167], v76, s[10:11]
	v_lshl_or_b32 v75, s21, 10, v194
	v_readlane_b32 s16, v231, 1
	v_readlane_b32 s18, v231, 2
	v_lshl_or_b32 v76, s20, 10, v194
	global_load_dwordx4 v[168:171], v75, s[10:11]
	global_load_dwordx4 v[172:175], v76, s[10:11]
	v_lshl_or_b32 v75, s19, 10, v194
	v_readlane_b32 s9, v231, 0
	v_lshl_or_b32 v76, s18, 10, v194
	global_load_dwordx4 v[176:179], v75, s[10:11]
	global_load_dwordx4 v[180:183], v76, s[10:11]
	v_lshl_or_b32 v75, s16, 10, v194
	v_lshl_or_b32 v76, s9, 10, v194
	global_load_dwordx4 v[184:187], v75, s[10:11]
	global_load_dwordx4 v[188:191], v76, s[10:11]
	v_and_b32_e32 v75, 1, v0
	v_lshrrev_b32_e32 v76, 2, v0
	v_and_b32_e32 v0, 3, v0
	v_and_or_b32 v193, v76, 12, v0
	v_cmp_eq_u32_e64 s[2:3], 0, v75
	v_mbcnt_lo_u32_b32 v0, -1, 0
	s_mov_b32 s9, 0x800000
	s_mov_b32 s16, 0x45800000
	s_mov_b32 s27, 0x42ee0000
	s_mov_b32 s28, 0x3e6d3388
	s_mov_b32 s29, 0xc040c00
	s_mov_b32 s30, 0xc050c01
	s_mov_b32 s31, 0xc060c02
	s_mov_b32 s33, 0xc070c03
	v_mbcnt_hi_u32_b32 v228, -1, v0
	s_mov_b32 s20, s8
	s_branch .LBB0_1014

.Lp10_nobar_i:
	v_dot8_i32_i4 v88, v248, v70, 0
	v_dot8_i32_i4 v88, v250, v71, v88
	s_nop 2
	v_lshlrev_b32_e32 v88, 4, v88
	v_dot8_i32_i4 v88, v247, v70, v88
	v_dot8_i32_i4 v74, v248, v188, 0
	v_dot8_i32_i4 v75, v248, v184, 0
	v_dot8_i32_i4 v76, v248, v180, 0
	v_dot8_i32_i4 v77, v248, v176, 0
	v_dot8_i32_i4 v78, v248, v172, 0
	v_dot8_i32_i4 v79, v248, v168, 0
	v_dot8_i32_i4 v80, v248, v164, 0
	v_dot8_i32_i4 v81, v248, v160, 0
	v_dot8_i32_i4 v82, v248, v156, 0
	v_dot8_i32_i4 v83, v248, v152, 0
	v_dot8_i32_i4 v84, v248, v148, 0
	v_dot8_i32_i4 v85, v248, v144, 0
	v_dot8_i32_i4 v86, v248, v116, 0
	v_dot8_i32_i4 v87, v248, v112, 0
	v_dot8_i32_i4 v70, v248, v66, 0
	v_dot8_i32_i4 v74, v250, v189, v74
	v_dot8_i32_i4 v75, v250, v185, v75
	v_dot8_i32_i4 v76, v250, v181, v76
	v_dot8_i32_i4 v77, v250, v177, v77
	v_dot8_i32_i4 v78, v250, v173, v78
	v_dot8_i32_i4 v79, v250, v169, v79
	v_dot8_i32_i4 v80, v250, v165, v80
	v_dot8_i32_i4 v81, v250, v161, v81
	v_dot8_i32_i4 v82, v250, v157, v82
	v_dot8_i32_i4 v83, v250, v153, v83
	v_dot8_i32_i4 v84, v250, v149, v84
	v_dot8_i32_i4 v85, v250, v145, v85
	v_dot8_i32_i4 v86, v250, v117, v86
	v_dot8_i32_i4 v87, v250, v113, v87
	v_dot8_i32_i4 v70, v250, v67, v70
	v_lshlrev_b32_e32 v74, 4, v74
	v_lshlrev_b32_e32 v75, 4, v75
	v_lshlrev_b32_e32 v76, 4, v76
	v_lshlrev_b32_e32 v77, 4, v77
	v_lshlrev_b32_e32 v78, 4, v78
	v_lshlrev_b32_e32 v79, 4, v79
	v_lshlrev_b32_e32 v80, 4, v80
	v_lshlrev_b32_e32 v81, 4, v81
	v_lshlrev_b32_e32 v82, 4, v82
	v_lshlrev_b32_e32 v83, 4, v83
	v_lshlrev_b32_e32 v84, 4, v84
	v_lshlrev_b32_e32 v85, 4, v85
	v_lshlrev_b32_e32 v86, 4, v86
	v_lshlrev_b32_e32 v87, 4, v87
	v_lshlrev_b32_e32 v70, 4, v70
	v_dot8_i32_i4 v74, v247, v188, v74
	v_dot8_i32_i4 v75, v247, v184, v75
	v_dot8_i32_i4 v76, v247, v180, v76
	v_dot8_i32_i4 v77, v247, v176, v77
	v_dot8_i32_i4 v78, v247, v172, v78
	v_dot8_i32_i4 v79, v247, v168, v79
	v_dot8_i32_i4 v80, v247, v164, v80
	v_dot8_i32_i4 v81, v247, v160, v81
	v_dot8_i32_i4 v82, v247, v156, v82
	v_dot8_i32_i4 v83, v247, v152, v83
	v_dot8_i32_i4 v84, v247, v148, v84
	v_dot8_i32_i4 v85, v247, v144, v85
	v_dot8_i32_i4 v86, v247, v116, v86
	v_dot8_i32_i4 v87, v247, v112, v87
	v_dot8_i32_i4 v70, v247, v66, v70
	v_dot8_i32_i4 v74, v249, v189, v74
	v_dot8_i32_i4 v75, v249, v185, v75
	v_dot8_i32_i4 v76, v249, v181, v76
	v_dot8_i32_i4 v77, v249, v177, v77
	v_dot8_i32_i4 v78, v249, v173, v78
	v_dot8_i32_i4 v79, v249, v169, v79
	v_dot8_i32_i4 v80, v249, v165, v80
	v_dot8_i32_i4 v81, v249, v161, v81
	v_dot8_i32_i4 v82, v249, v157, v82
	v_dot8_i32_i4 v83, v249, v153, v83
	v_dot8_i32_i4 v84, v249, v149, v84
	v_dot8_i32_i4 v85, v249, v145, v85
	v_dot8_i32_i4 v86, v249, v117, v86
	v_dot8_i32_i4 v87, v249, v113, v87
	v_dot8_i32_i4 v88, v249, v71, v88
	v_dot8_i32_i4 v70, v249, v67, v70
	v_permlane32_swap_b32_e32 v74, v82
	v_permlane32_swap_b32_e32 v75, v83
	v_permlane32_swap_b32_e32 v76, v84
	v_permlane32_swap_b32_e32 v77, v85
	v_permlane32_swap_b32_e32 v78, v86
	v_permlane32_swap_b32_e32 v79, v87
	v_permlane32_swap_b32_e32 v80, v88
	v_permlane32_swap_b32_e32 v81, v70
	v_add_u32_e32 v66, v74, v82
	v_add_u32_e32 v67, v75, v83
	v_add_u32_e32 v71, v76, v84
	v_add_u32_e32 v74, v77, v85
	v_add_u32_e32 v75, v78, v86
	v_add_u32_e32 v76, v79, v87
	v_add_u32_e32 v77, v80, v88
	v_add_u32_e32 v70, v81, v70
	v_permlane16_swap_b32_e32 v66, v75
	v_permlane16_swap_b32_e32 v67, v76
	v_permlane16_swap_b32_e32 v71, v77
	v_permlane16_swap_b32_e32 v74, v70
	v_add_u32_e32 v66, v66, v75
	v_add_u32_e32 v67, v67, v76
	v_add_u32_e32 v71, v71, v77
	v_add_u32_e32 v70, v74, v70
	v_cndmask_b32_e64 v74, v71, v66, s[0:1]
	v_cndmask_b32_e64 v66, v66, v71, s[0:1]
	v_cndmask_b32_e64 v71, v70, v67, s[0:1]
	v_cndmask_b32_e64 v67, v67, v70, s[0:1]
	v_add_u32_dpp v66, v66, v74 quad_perm:[2,3,0,1] row_mask:0xf bank_mask:0xf bound_ctrl:1
	s_sub_i32 s4, s21, 32
	v_add_u32_dpp v67, v67, v71 quad_perm:[2,3,0,1] row_mask:0xf bank_mask:0xf bound_ctrl:1
	v_cndmask_b32_e64 v70, v67, v66, s[2:3]
	v_cndmask_b32_e64 v66, v66, v67, s[2:3]
	s_cmp_lt_u32 s25, 4
	s_cselect_b64 vcc, -1, 0
	v_add_u32_dpp v66, v66, v70 quad_perm:[1,0,3,2] row_mask:0xf bank_mask:0xf bound_ctrl:1
	v_cndmask_b32_e32 v70, v234, v233, vcc
	v_cndmask_b32_e32 v71, v230, v229, vcc
	v_add_u32_dpp v66, v66, v66 row_ror:8 row_mask:0xf bank_mask:0xf bound_ctrl:1
	s_cmp_eq_u32 s21, 32
	s_nop 0
	v_add_u32_dpp v67, v66, v66 row_ror:4 row_mask:0xf bank_mask:0xf bound_ctrl:1
	v_and_or_b32 v66, s4, 32, v193
	v_lshlrev_b32_e32 v66, 2, v66
	v_cvt_f32_i32_e32 v74, v67
	ds_bpermute_b32 v75, v66, v70
	v_and_b32_e32 v67, 0xffff0000, v71
	ds_bpermute_b32 v76, v66, v67
	v_add_f32_e32 v71, v251, v74
	v_mul_f32_e32 v71, v244, v71
	s_waitcnt lgkmcnt(1)
	v_mul_f32_e32 v74, v71, v75
	v_fma_f32 v71, |v74|, s28, 1.0
	v_rcp_f32_e32 v75, v71
	v_mul_f32_e32 v79, v74, v74
	v_mul_f32_e32 v79, 0xbf38aa3b, v79
	v_exp_f32_e32 v79, v79
	v_fmamk_f32 v78, v75, 0x3f07dc22, v227
	v_fmaak_f32 v78, v75, v78, 0x3f35f0e3
	v_fmaak_f32 v78, v75, v78, 0xbe11a98e
	v_cndmask_b32_e32 v71, v236, v235, vcc
	v_fmaak_f32 v78, v75, v78, 0x3e027906
	ds_bpermute_b32 v77, v66, v71
	v_mul_f32_e32 v75, v75, v78
	v_mul_f32_e32 v75, v79, v75
	v_mul_f32_e32 v78, v74, v75
	v_fma_f32 v75, -v74, v75, v74
	v_cmp_gt_f32_e32 vcc, 0, v74
	s_nop 1
	v_cndmask_b32_e32 v74, v75, v78, vcc
	s_waitcnt lgkmcnt(1)
	v_mul_f32_e32 v74, v74, v76
	s_cselect_b64 vcc, -1, 0
	s_cmp_gt_u32 s25, 5
	s_waitcnt lgkmcnt(0)
; __device__ __forceinline__ void expert_tokens(const unsigned char* __restrict__ UV, const float* __restrict__ US, const float* __restrict__ VS, ...
;     ...
;         const unsigned nw0 = (unsigned)IDX[(size_t)tn * 128 + lane], nw1 = (unsigned)IDX[(size_t)tn * 128 + 64 + lane];
;         const int ni0 = (int)nw0 & rmask, ni1 = (int)nw1 & rmask;
	v_mul_f32_e32 v74, v74, v77
	s_cselect_b64 s[22:23], -1, 0
	s_cmp_lt_u32 s25, 6
	v_fma_mixlo_f16 v116, v74, s16, 0
	s_cselect_b64 s[4:5], -1, 0
	v_and_b32_e32 v117, 0xffff, v116
	v_cndmask_b32_e64 v74, v242, v232, s[4:5]
	s_add_i32 s24, s21, 1
	s_add_i32 s35, s21, 2
	s_add_i32 s36, s21, 3
	s_add_i32 s37, s21, 4
	s_add_i32 s38, s21, 5
	s_add_i32 s39, s21, 6
	s_add_i32 s40, s21, 7
	s_add_i32 s49, s21, 8
	s_add_i32 s50, s21, 9
	s_add_i32 s51, s21, 10
	s_add_i32 s52, s21, 11
	s_add_i32 s53, s21, 12
	s_add_i32 s54, s21, 13
	s_add_i32 s55, s21, 14
	s_add_i32 s56, s21, 15
	v_cndmask_b32_e32 v136, v74, v231, vcc
	v_mov_b32_dpp v207, v117 quad_perm:[1,0,3,2] row_mask:0xf bank_mask:0xf
	v_lshlrev_b32_e32 v136, 10, v136
	s_cmp_lg_u32 s21, 32
	v_readlane_b32 s61, v136, s21
	v_readlane_b32 s62, v136, s24
	v_readlane_b32 s63, v136, s35
	v_readlane_b32 s64, v136, s36
	v_readlane_b32 s65, v136, s37
	v_readlane_b32 s66, v136, s38
	v_readlane_b32 s67, v136, s39
	v_readlane_b32 s68, v136, s40
	v_readlane_b32 s69, v136, s49
	v_readlane_b32 s70, v136, s50
	v_readlane_b32 s71, v136, s51
	v_readlane_b32 s72, v136, s52
	v_readlane_b32 s73, v136, s53
	v_readlane_b32 s74, v136, s54
	v_readlane_b32 s75, v136, s55
	v_readlane_b32 s76, v136, s56
	v_lshl_or_b32 v209, v207, 16, v117
	s_nop 0
	v_readlane_b32 s47, v209, 0
	v_readlane_b32 s45, v209, 2
	v_readlane_b32 s43, v209, 16
	v_readlane_b32 s41, v209, 18
	v_readlane_b32 s39, v209, 32
	v_readlane_b32 s37, v209, 34
	v_readlane_b32 s35, v209, 48
	v_readlane_b32 s4, v209, 50
	buffer_load_dwordx4 v[78:81], v194, s[80:83], s61 offen
	buffer_load_dwordx4 v[74:77], v194, s[80:83], s62 offen
	buffer_load_dwordx4 v[86:89], v194, s[80:83], s63 offen
	buffer_load_dwordx4 v[82:85], v194, s[80:83], s64 offen
	buffer_load_dwordx4 v[94:97], v194, s[80:83], s65 offen
	buffer_load_dwordx4 v[90:93], v194, s[80:83], s66 offen
	buffer_load_dwordx4 v[102:105], v194, s[80:83], s67 offen
	buffer_load_dwordx4 v[98:101], v194, s[80:83], s68 offen
	buffer_load_dwordx4 v[110:113], v194, s[80:83], s69 offen
	buffer_load_dwordx4 v[106:109], v194, s[80:83], s70 offen
	buffer_load_dwordx4 v[124:127], v194, s[80:83], s71 offen
	buffer_load_dwordx4 v[120:123], v194, s[80:83], s72 offen
	buffer_load_dwordx4 v[132:135], v194, s[80:83], s73 offen
	buffer_load_dwordx4 v[128:131], v194, s[80:83], s74 offen
	buffer_load_dwordx4 v[140:143], v194, s[80:83], s75 offen
	buffer_load_dwordx4 v[136:139], v194, s[80:83], s76 offen
	s_cbranch_scc1 .LBB0_1021
	s_waitcnt vmcnt(16)
	s_bfe_i32 s60, s34, 0x10000
	v_alignbit_b32 v237, v237, v237, 16
	v_alignbit_b32 v238, v238, v238, 16
	v_xor_b32_e32 v237, s60, v237
	v_xor_b32_e32 v238, s60, v238
	s_nop 1
	s_mov_b32 s58, 0x99999999
	s_mov_b32 s59, 0x99999999
	v_min_u32_dpp v202, v237, v237 quad_perm:[1,0,3,2] row_mask:0xf bank_mask:0xf
	v_max_u32_dpp v203, v237, v237 quad_perm:[1,0,3,2] row_mask:0xf bank_mask:0xf
	v_min_u32_dpp v204, v238, v238 quad_perm:[1,0,3,2] row_mask:0xf bank_mask:0xf
	v_max_u32_dpp v205, v238, v238 quad_perm:[1,0,3,2] row_mask:0xf bank_mask:0xf
	v_cndmask_b32_e64 v237, v203, v202, s[58:59]
	v_cndmask_b32_e64 v238, v205, v204, s[58:59]
	s_mov_b32 s58, 0xcc33cc33
	s_mov_b32 s59, 0xcc33cc33
	v_min_u32_dpp v202, v237, v237 quad_perm:[2,3,0,1] row_mask:0xf bank_mask:0xf
	v_max_u32_dpp v203, v237, v237 quad_perm:[2,3,0,1] row_mask:0xf bank_mask:0xf
	v_min_u32_dpp v204, v238, v238 quad_perm:[2,3,0,1] row_mask:0xf bank_mask:0xf
	v_max_u32_dpp v205, v238, v238 quad_perm:[2,3,0,1] row_mask:0xf bank_mask:0xf
	v_cndmask_b32_e64 v237, v203, v202, s[58:59]
	v_cndmask_b32_e64 v238, v205, v204, s[58:59]
	s_mov_b32 s58, 0xaa55aa55
	s_mov_b32 s59, 0xaa55aa55
	v_min_u32_dpp v202, v237, v237 quad_perm:[1,0,3,2] row_mask:0xf bank_mask:0xf
	v_max_u32_dpp v203, v237, v237 quad_perm:[1,0,3,2] row_mask:0xf bank_mask:0xf
	v_min_u32_dpp v204, v238, v238 quad_perm:[1,0,3,2] row_mask:0xf bank_mask:0xf
	v_max_u32_dpp v205, v238, v238 quad_perm:[1,0,3,2] row_mask:0xf bank_mask:0xf
	v_cndmask_b32_e64 v237, v203, v202, s[58:59]
	v_cndmask_b32_e64 v238, v205, v204, s[58:59]
	s_mov_b32 s58, 0xf00ff00f
	s_mov_b32 s59, 0xf00ff00f
	v_min_u32_dpp v202, v237, v237 row_ror:8 row_mask:0xf bank_mask:0xf
	v_max_u32_dpp v203, v237, v237 row_ror:8 row_mask:0xf bank_mask:0xf
	v_min_u32_dpp v204, v238, v238 row_ror:8 row_mask:0xf bank_mask:0xf
	v_max_u32_dpp v205, v238, v238 row_ror:8 row_mask:0xf bank_mask:0xf
	v_cndmask_b32_e64 v237, v203, v202, s[58:59]
	v_cndmask_b32_e64 v238, v205, v204, s[58:59]
	s_mov_b32 s58, 0xc3c3c3c3
	s_mov_b32 s59, 0xc3c3c3c3
	v_min_u32_dpp v202, v237, v237 quad_perm:[2,3,0,1] row_mask:0xf bank_mask:0xf
	v_max_u32_dpp v203, v237, v237 quad_perm:[2,3,0,1] row_mask:0xf bank_mask:0xf
	v_min_u32_dpp v204, v238, v238 quad_perm:[2,3,0,1] row_mask:0xf bank_mask:0xf
	v_max_u32_dpp v205, v238, v238 quad_perm:[2,3,0,1] row_mask:0xf bank_mask:0xf
	v_cndmask_b32_e64 v237, v203, v202, s[58:59]
	v_cndmask_b32_e64 v238, v205, v204, s[58:59]
	s_mov_b32 s58, 0xa5a5a5a5
	s_mov_b32 s59, 0xa5a5a5a5
	v_min_u32_dpp v202, v237, v237 quad_perm:[1,0,3,2] row_mask:0xf bank_mask:0xf
	v_max_u32_dpp v203, v237, v237 quad_perm:[1,0,3,2] row_mask:0xf bank_mask:0xf
	v_min_u32_dpp v204, v238, v238 quad_perm:[1,0,3,2] row_mask:0xf bank_mask:0xf
	v_max_u32_dpp v205, v238, v238 quad_perm:[1,0,3,2] row_mask:0xf bank_mask:0xf
	v_cndmask_b32_e64 v237, v203, v202, s[58:59]
	v_cndmask_b32_e64 v238, v205, v204, s[58:59]
	s_mov_b32 s58, 0xf0f00f0f
	s_mov_b32 s59, 0xf0f00f0f
	v_mov_b32_dpp v202, v237 row_half_mirror row_mask:0xf bank_mask:0xf
	v_mov_b32_dpp v204, v238 row_half_mirror row_mask:0xf bank_mask:0xf
	s_nop 0
; __device__ __forceinline__ void expert_tokens(const unsigned char* __restrict__ UV, const float* __restrict__ US, const float* __restrict__ VS, ...
;     ...
;         const unsigned nw0 = (unsigned)IDX[(size_t)tn * 128 + lane], nw1 = (unsigned)IDX[(size_t)tn * 128 + 64 + lane];
;         const int ni0 = (int)nw0 & rmask, ni1 = (int)nw1 & rmask;
;         const float ng0 = __uint_as_float(nw0 & 0xFFFF0000u), ng1 = __uint_as_float(nw1 & 0xFFFF0000u);
	v_max_u32_dpp v203, v202, v237 quad_perm:[3,2,1,0] row_mask:0xf bank_mask:0xf
	v_max_u32_dpp v205, v204, v238 quad_perm:[3,2,1,0] row_mask:0xf bank_mask:0xf
	v_min_u32_dpp v202, v202, v237 quad_perm:[3,2,1,0] row_mask:0xf bank_mask:0xf
	v_min_u32_dpp v204, v204, v238 quad_perm:[3,2,1,0] row_mask:0xf bank_mask:0xf
	v_cndmask_b32_e64 v237, v203, v202, s[58:59]
	v_cndmask_b32_e64 v238, v205, v204, s[58:59]
	s_mov_b32 s58, 0xff0000ff
	s_mov_b32 s59, 0xff0000ff
	v_min_u32_dpp v202, v237, v237 row_ror:8 row_mask:0xf bank_mask:0xf
	v_max_u32_dpp v203, v237, v237 row_ror:8 row_mask:0xf bank_mask:0xf
	v_min_u32_dpp v204, v238, v238 row_ror:8 row_mask:0xf bank_mask:0xf
	v_max_u32_dpp v205, v238, v238 row_ror:8 row_mask:0xf bank_mask:0xf
	v_cndmask_b32_e64 v237, v203, v202, s[58:59]
	v_cndmask_b32_e64 v238, v205, v204, s[58:59]
	s_mov_b32 s58, 0xcccc3333
	s_mov_b32 s59, 0xcccc3333
	v_min_u32_dpp v202, v237, v237 quad_perm:[2,3,0,1] row_mask:0xf bank_mask:0xf
	v_max_u32_dpp v203, v237, v237 quad_perm:[2,3,0,1] row_mask:0xf bank_mask:0xf
	v_min_u32_dpp v204, v238, v238 quad_perm:[2,3,0,1] row_mask:0xf bank_mask:0xf
	v_max_u32_dpp v205, v238, v238 quad_perm:[2,3,0,1] row_mask:0xf bank_mask:0xf
	v_cndmask_b32_e64 v237, v203, v202, s[58:59]
	v_cndmask_b32_e64 v238, v205, v204, s[58:59]
	s_mov_b32 s58, 0xaaaa5555
	s_mov_b32 s59, 0xaaaa5555
	v_min_u32_dpp v202, v237, v237 quad_perm:[1,0,3,2] row_mask:0xf bank_mask:0xf
	v_max_u32_dpp v203, v237, v237 quad_perm:[1,0,3,2] row_mask:0xf bank_mask:0xf
	v_min_u32_dpp v204, v238, v238 quad_perm:[1,0,3,2] row_mask:0xf bank_mask:0xf
	v_max_u32_dpp v205, v238, v238 quad_perm:[1,0,3,2] row_mask:0xf bank_mask:0xf
	v_cndmask_b32_e64 v237, v203, v202, s[58:59]
	v_cndmask_b32_e64 v238, v205, v204, s[58:59]
	s_nop 1
	v_permlane16_swap_b32_e32 v237, v238
	s_mov_b32 s58, -1
	s_mov_b32 s59, 0
	v_min_u32_e32 v202, v237, v238
	v_max_u32_e32 v203, v237, v238
	v_cndmask_b32_e64 v237, v203, v202, s[58:59]
	v_cndmask_b32_e64 v238, v202, v203, s[58:59]
	s_mov_b32 s58, 0xf0f0f0f
	s_mov_b32 s59, 0xf0f0f0f0
	v_mov_b32_dpp v202, v237 row_half_mirror row_mask:0xf bank_mask:0xf
	v_mov_b32_dpp v204, v238 row_half_mirror row_mask:0xf bank_mask:0xf
	s_nop 0
	v_max_u32_dpp v203, v202, v237 quad_perm:[3,2,1,0] row_mask:0xf bank_mask:0xf
	v_max_u32_dpp v205, v204, v238 quad_perm:[3,2,1,0] row_mask:0xf bank_mask:0xf
	v_min_u32_dpp v202, v202, v237 quad_perm:[3,2,1,0] row_mask:0xf bank_mask:0xf
	v_min_u32_dpp v204, v204, v238 quad_perm:[3,2,1,0] row_mask:0xf bank_mask:0xf
	v_cndmask_b32_e64 v237, v203, v202, s[58:59]
	v_cndmask_b32_e64 v238, v205, v204, s[58:59]
	s_mov_b32 s58, 0xff00ff
	s_mov_b32 s59, 0xff00ff00
	v_min_u32_dpp v202, v237, v237 row_ror:8 row_mask:0xf bank_mask:0xf
	v_max_u32_dpp v203, v237, v237 row_ror:8 row_mask:0xf bank_mask:0xf
	v_min_u32_dpp v204, v238, v238 row_ror:8 row_mask:0xf bank_mask:0xf
	v_max_u32_dpp v205, v238, v238 row_ror:8 row_mask:0xf bank_mask:0xf
	v_cndmask_b32_e64 v237, v203, v202, s[58:59]
	v_cndmask_b32_e64 v238, v205, v204, s[58:59]
	s_mov_b32 s58, 0x33333333
	s_mov_b32 s59, 0xcccccccc
	v_min_u32_dpp v202, v237, v237 quad_perm:[2,3,0,1] row_mask:0xf bank_mask:0xf
	v_max_u32_dpp v203, v237, v237 quad_perm:[2,3,0,1] row_mask:0xf bank_mask:0xf
	v_min_u32_dpp v204, v238, v238 quad_perm:[2,3,0,1] row_mask:0xf bank_mask:0xf
	v_max_u32_dpp v205, v238, v238 quad_perm:[2,3,0,1] row_mask:0xf bank_mask:0xf
	v_cndmask_b32_e64 v237, v203, v202, s[58:59]
	v_cndmask_b32_e64 v238, v205, v204, s[58:59]
	s_mov_b32 s58, 0x55555555
	s_mov_b32 s59, 0xaaaaaaaa
	v_min_u32_dpp v202, v237, v237 quad_perm:[1,0,3,2] row_mask:0xf bank_mask:0xf
	v_max_u32_dpp v203, v237, v237 quad_perm:[1,0,3,2] row_mask:0xf bank_mask:0xf
	v_min_u32_dpp v204, v238, v238 quad_perm:[1,0,3,2] row_mask:0xf bank_mask:0xf
	v_max_u32_dpp v205, v238, v238 quad_perm:[1,0,3,2] row_mask:0xf bank_mask:0xf
	v_cndmask_b32_e64 v237, v203, v202, s[58:59]
	v_cndmask_b32_e64 v238, v205, v204, s[58:59]
	s_nop 1
	v_permlane32_swap_b32_e32 v237, v238
	s_mov_b32 s58, 0xffff
	s_mov_b32 s59, 0xffff
	v_min_u32_e32 v202, v237, v238
	v_max_u32_e32 v203, v237, v238
	v_cndmask_b32_e64 v237, v203, v202, s[58:59]
	v_cndmask_b32_e64 v238, v202, v203, s[58:59]
	s_nop 1
	v_permlane32_swap_b32_e32 v237, v238
	s_mov_b32 s58, 0xffff
	s_mov_b32 s59, 0xffff
	v_min_u32_e32 v202, v237, v238
	v_max_u32_e32 v203, v237, v238
	v_cndmask_b32_e64 v237, v203, v202, s[58:59]
	v_cndmask_b32_e64 v238, v202, v203, s[58:59]
	s_mov_b32 s58, 0xf0f00f0f
	s_mov_b32 s59, 0xf0f00f0f
	v_mov_b32_dpp v202, v237 row_half_mirror row_mask:0xf bank_mask:0xf
	v_mov_b32_dpp v204, v238 row_half_mirror row_mask:0xf bank_mask:0xf
	s_nop 0
	v_max_u32_dpp v203, v202, v237 quad_perm:[3,2,1,0] row_mask:0xf bank_mask:0xf
	v_max_u32_dpp v205, v204, v238 quad_perm:[3,2,1,0] row_mask:0xf bank_mask:0xf
	v_min_u32_dpp v202, v202, v237 quad_perm:[3,2,1,0] row_mask:0xf bank_mask:0xf
	v_min_u32_dpp v204, v204, v238 quad_perm:[3,2,1,0] row_mask:0xf bank_mask:0xf
	v_cndmask_b32_e64 v237, v203, v202, s[58:59]
	v_cndmask_b32_e64 v238, v205, v204, s[58:59]
	s_mov_b32 s58, 0xff0000ff
	s_mov_b32 s59, 0xff0000ff
	v_min_u32_dpp v202, v237, v237 row_ror:8 row_mask:0xf bank_mask:0xf
	v_max_u32_dpp v203, v237, v237 row_ror:8 row_mask:0xf bank_mask:0xf
	v_min_u32_dpp v204, v238, v238 row_ror:8 row_mask:0xf bank_mask:0xf
	v_max_u32_dpp v205, v238, v238 row_ror:8 row_mask:0xf bank_mask:0xf
	v_cndmask_b32_e64 v237, v203, v202, s[58:59]
	v_cndmask_b32_e64 v238, v205, v204, s[58:59]
	s_mov_b32 s58, 0xcccc3333
	s_mov_b32 s59, 0xcccc3333
	v_min_u32_dpp v202, v237, v237 quad_perm:[2,3,0,1] row_mask:0xf bank_mask:0xf
; __device__ __forceinline__ void expert_tokens(const unsigned char* __restrict__ UV, const float* __restrict__ US, const float* __restrict__ VS, ...
;     ...
;         const unsigned nw0 = (unsigned)IDX[(size_t)tn * 128 + lane], nw1 = (unsigned)IDX[(size_t)tn * 128 + 64 + lane];
;         const int ni0 = (int)nw0 & rmask, ni1 = (int)nw1 & rmask;
;         const float ng0 = __uint_as_float(nw0 & 0xFFFF0000u), ng1 = __uint_as_float(nw1 & 0xFFFF0000u);
	v_max_u32_dpp v203, v237, v237 quad_perm:[2,3,0,1] row_mask:0xf bank_mask:0xf
	v_min_u32_dpp v204, v238, v238 quad_perm:[2,3,0,1] row_mask:0xf bank_mask:0xf
	v_max_u32_dpp v205, v238, v238 quad_perm:[2,3,0,1] row_mask:0xf bank_mask:0xf
	v_cndmask_b32_e64 v237, v203, v202, s[58:59]
	v_cndmask_b32_e64 v238, v205, v204, s[58:59]
	s_mov_b32 s58, 0xaaaa5555
	s_mov_b32 s59, 0xaaaa5555
	v_min_u32_dpp v202, v237, v237 quad_perm:[1,0,3,2] row_mask:0xf bank_mask:0xf
	v_max_u32_dpp v203, v237, v237 quad_perm:[1,0,3,2] row_mask:0xf bank_mask:0xf
	v_min_u32_dpp v204, v238, v238 quad_perm:[1,0,3,2] row_mask:0xf bank_mask:0xf
	v_max_u32_dpp v205, v238, v238 quad_perm:[1,0,3,2] row_mask:0xf bank_mask:0xf
	v_cndmask_b32_e64 v237, v203, v202, s[58:59]
	v_cndmask_b32_e64 v238, v205, v204, s[58:59]
	s_nop 1
	v_permlane16_swap_b32_e32 v237, v238
	v_min_u32_e32 v202, v237, v238
	v_max_u32_e32 v238, v237, v238
	v_mov_b32_e32 v237, v202
	s_nop 1
	v_permlane32_swap_b32_e32 v237, v238
	v_min_u32_e32 v202, v237, v238
	v_max_u32_e32 v238, v237, v238
	v_mov_b32_e32 v237, v202
	s_nop 1
	v_permlane16_swap_b32_e32 v237, v238
	v_min_u32_e32 v202, v237, v238
	v_max_u32_e32 v238, v237, v238
	v_mov_b32_e32 v237, v202
	s_nop 1
	v_permlane16_swap_b32_e32 v237, v238
	s_nop 1
	v_permlane32_swap_b32_e32 v237, v238
	v_xor_b32_e32 v237, s60, v237
	v_xor_b32_e32 v238, s60, v238
	v_alignbit_b32 v237, v237, v237, 16
	v_alignbit_b32 v238, v238, v238, 16
	v_and_b32_e32 v242, 0x3fff, v237
	v_and_b32_e32 v243, 0x3fff, v238
	v_lshlrev_b32_e32 v208, 2, v242
	v_lshlrev_b32_e32 v206, 2, v243
	global_load_dword v241, v208, s[12:13]
	global_load_dword v0, v206, s[12:13]
	global_load_dword v245, v208, s[14:15]
	global_load_dword v246, v206, s[14:15]
.LBB0_1021:
	v_perm_b32 v149, v186, v190, s29
	v_dot2c_f32_f16_e32 v224, s47, v149
	v_and_b32_e32 v149, s32, v149
	v_dot2c_f32_f16_e32 v220, s47, v149
	v_perm_b32 v149, v186, v190, s30
	v_dot2c_f32_f16_e32 v225, s47, v149
	v_and_b32_e32 v149, s32, v149
	v_dot2c_f32_f16_e32 v221, s47, v149
	v_perm_b32 v149, v186, v190, s31
	v_perm_b32 v117, v186, v190, s33
	v_dot2c_f32_f16_e32 v223, s47, v117
	v_and_b32_e32 v117, s32, v117
	v_dot2c_f32_f16_e32 v222, s47, v149
	v_and_b32_e32 v149, s32, v149
	v_dot2c_f32_f16_e32 v219, s47, v117
	v_dot2c_f32_f16_e32 v218, s47, v149
	v_perm_b32 v149, v187, v191, s29
	v_dot2c_f32_f16_e32 v216, s47, v149
	v_and_b32_e32 v149, s32, v149
	v_dot2c_f32_f16_e32 v212, s47, v149
	v_perm_b32 v149, v187, v191, s30
	v_dot2c_f32_f16_e32 v217, s47, v149
	v_and_b32_e32 v149, s32, v149
	v_dot2c_f32_f16_e32 v213, s47, v149
	v_perm_b32 v149, v187, v191, s31
	v_perm_b32 v117, v187, v191, s33
	v_dot2c_f32_f16_e32 v215, s47, v117
	v_and_b32_e32 v117, s32, v117
	v_dot2c_f32_f16_e32 v214, s47, v149
	v_and_b32_e32 v149, s32, v149
	v_dot2c_f32_f16_e32 v211, s47, v117
	v_dot2c_f32_f16_e32 v210, s47, v149
	v_perm_b32 v149, v178, v182, s29
	v_dot2c_f32_f16_e32 v224, s45, v149
	v_and_b32_e32 v149, s32, v149
	v_dot2c_f32_f16_e32 v220, s45, v149
	v_perm_b32 v149, v178, v182, s30
	v_dot2c_f32_f16_e32 v225, s45, v149
	v_and_b32_e32 v149, s32, v149
	v_dot2c_f32_f16_e32 v221, s45, v149
	v_perm_b32 v149, v178, v182, s31
	v_perm_b32 v117, v178, v182, s33
	v_dot2c_f32_f16_e32 v223, s45, v117
	v_and_b32_e32 v117, s32, v117
	v_dot2c_f32_f16_e32 v222, s45, v149
	v_and_b32_e32 v149, s32, v149
	v_dot2c_f32_f16_e32 v219, s45, v117
	v_dot2c_f32_f16_e32 v218, s45, v149
	v_perm_b32 v149, v179, v183, s29
	v_dot2c_f32_f16_e32 v216, s45, v149
	v_and_b32_e32 v149, s32, v149
	v_dot2c_f32_f16_e32 v212, s45, v149
	v_perm_b32 v149, v179, v183, s30
	v_dot2c_f32_f16_e32 v217, s45, v149
	v_and_b32_e32 v149, s32, v149
	v_dot2c_f32_f16_e32 v213, s45, v149
	v_perm_b32 v149, v179, v183, s31
	v_perm_b32 v117, v179, v183, s33
	v_dot2c_f32_f16_e32 v215, s45, v117
	v_and_b32_e32 v117, s32, v117
	v_dot2c_f32_f16_e32 v214, s45, v149
	v_and_b32_e32 v149, s32, v149
	v_dot2c_f32_f16_e32 v211, s45, v117
	v_dot2c_f32_f16_e32 v210, s45, v149
	v_perm_b32 v149, v170, v174, s29
	v_dot2c_f32_f16_e32 v224, s43, v149
	v_and_b32_e32 v149, s32, v149
	v_dot2c_f32_f16_e32 v220, s43, v149
	v_perm_b32 v149, v170, v174, s30
	v_dot2c_f32_f16_e32 v225, s43, v149
	v_and_b32_e32 v149, s32, v149
	v_dot2c_f32_f16_e32 v221, s43, v149
	v_perm_b32 v149, v170, v174, s31
	v_perm_b32 v117, v170, v174, s33
	v_dot2c_f32_f16_e32 v223, s43, v117
	v_and_b32_e32 v117, s32, v117
	v_dot2c_f32_f16_e32 v222, s43, v149
	v_and_b32_e32 v149, s32, v149
	v_dot2c_f32_f16_e32 v219, s43, v117
	v_dot2c_f32_f16_e32 v218, s43, v149
	v_perm_b32 v149, v171, v175, s29
	v_dot2c_f32_f16_e32 v216, s43, v149
	v_and_b32_e32 v149, s32, v149
	v_dot2c_f32_f16_e32 v212, s43, v149
	v_perm_b32 v149, v171, v175, s30
	v_dot2c_f32_f16_e32 v217, s43, v149
	v_and_b32_e32 v149, s32, v149
	v_dot2c_f32_f16_e32 v213, s43, v149
	v_perm_b32 v149, v171, v175, s31
	v_perm_b32 v117, v171, v175, s33
	v_dot2c_f32_f16_e32 v215, s43, v117
	v_and_b32_e32 v117, s32, v117
	v_dot2c_f32_f16_e32 v214, s43, v149
	v_and_b32_e32 v149, s32, v149
	v_dot2c_f32_f16_e32 v211, s43, v117
	v_dot2c_f32_f16_e32 v210, s43, v149
	v_perm_b32 v149, v162, v166, s29
	v_dot2c_f32_f16_e32 v224, s41, v149
	v_and_b32_e32 v149, s32, v149
	v_dot2c_f32_f16_e32 v220, s41, v149
	v_perm_b32 v149, v162, v166, s30
	v_dot2c_f32_f16_e32 v225, s41, v149
	v_and_b32_e32 v149, s32, v149
	v_dot2c_f32_f16_e32 v221, s41, v149
	v_perm_b32 v149, v162, v166, s31
	v_perm_b32 v117, v162, v166, s33
	v_dot2c_f32_f16_e32 v223, s41, v117
	v_and_b32_e32 v117, s32, v117
	v_dot2c_f32_f16_e32 v222, s41, v149
	v_and_b32_e32 v149, s32, v149
	v_dot2c_f32_f16_e32 v219, s41, v117
	v_dot2c_f32_f16_e32 v218, s41, v149
	v_perm_b32 v149, v163, v167, s29
	v_dot2c_f32_f16_e32 v216, s41, v149
	v_and_b32_e32 v149, s32, v149
	v_dot2c_f32_f16_e32 v212, s41, v149
	v_perm_b32 v149, v163, v167, s30
	v_dot2c_f32_f16_e32 v217, s41, v149
	v_and_b32_e32 v149, s32, v149
	v_dot2c_f32_f16_e32 v213, s41, v149
	v_perm_b32 v149, v163, v167, s31
	v_perm_b32 v117, v163, v167, s33
	v_dot2c_f32_f16_e32 v215, s41, v117
	v_and_b32_e32 v117, s32, v117
	v_dot2c_f32_f16_e32 v214, s41, v149
	v_and_b32_e32 v149, s32, v149
	v_dot2c_f32_f16_e32 v211, s41, v117
	v_dot2c_f32_f16_e32 v210, s41, v149
	v_perm_b32 v149, v154, v158, s29
	v_dot2c_f32_f16_e32 v224, s39, v149
	v_and_b32_e32 v149, s32, v149
	v_dot2c_f32_f16_e32 v220, s39, v149
	v_perm_b32 v149, v154, v158, s30
	v_dot2c_f32_f16_e32 v225, s39, v149
	v_and_b32_e32 v149, s32, v149
	v_dot2c_f32_f16_e32 v221, s39, v149
	v_perm_b32 v149, v154, v158, s31
	v_perm_b32 v117, v154, v158, s33
	v_dot2c_f32_f16_e32 v223, s39, v117
	v_and_b32_e32 v117, s32, v117
	v_dot2c_f32_f16_e32 v222, s39, v149
	v_and_b32_e32 v149, s32, v149
	v_dot2c_f32_f16_e32 v219, s39, v117
	v_dot2c_f32_f16_e32 v218, s39, v149
	v_perm_b32 v149, v155, v159, s29
	v_dot2c_f32_f16_e32 v216, s39, v149
	v_and_b32_e32 v149, s32, v149
	v_dot2c_f32_f16_e32 v212, s39, v149
	v_perm_b32 v149, v155, v159, s30
	v_dot2c_f32_f16_e32 v217, s39, v149
	v_and_b32_e32 v149, s32, v149
	v_dot2c_f32_f16_e32 v213, s39, v149
	v_perm_b32 v149, v155, v159, s31
	v_perm_b32 v117, v155, v159, s33
	v_dot2c_f32_f16_e32 v215, s39, v117
	v_and_b32_e32 v117, s32, v117
	v_dot2c_f32_f16_e32 v214, s39, v149
	v_and_b32_e32 v149, s32, v149
	v_dot2c_f32_f16_e32 v211, s39, v117
	v_perm_b32 v148, v146, v150, s29
	v_dot2c_f32_f16_e32 v224, s37, v148
	v_and_b32_e32 v148, s32, v148
	v_dot2c_f32_f16_e32 v220, s37, v148
	v_perm_b32 v148, v146, v150, s30
	v_dot2c_f32_f16_e32 v225, s37, v148
	v_and_b32_e32 v148, s32, v148
	v_dot2c_f32_f16_e32 v221, s37, v148
	v_perm_b32 v148, v146, v150, s31
	v_perm_b32 v117, v146, v150, s33
	v_dot2c_f32_f16_e32 v223, s37, v117
	v_and_b32_e32 v117, s32, v117
	v_dot2c_f32_f16_e32 v222, s37, v148
	v_and_b32_e32 v148, s32, v148
	v_dot2c_f32_f16_e32 v219, s37, v117
	v_perm_b32 v207, v147, v151, s29
	v_dot2c_f32_f16_e32 v216, s37, v207
	v_and_b32_e32 v207, s32, v207
	v_dot2c_f32_f16_e32 v212, s37, v207
	v_perm_b32 v207, v147, v151, s30
	v_dot2c_f32_f16_e32 v217, s37, v207
	v_and_b32_e32 v207, s32, v207
	v_dot2c_f32_f16_e32 v213, s37, v207
	v_perm_b32 v207, v147, v151, s31
	v_perm_b32 v117, v147, v151, s33
	v_dot2c_f32_f16_e32 v215, s37, v117
	v_and_b32_e32 v117, s32, v117
	v_dot2c_f32_f16_e32 v214, s37, v207
	v_and_b32_e32 v207, s32, v207
	v_dot2c_f32_f16_e32 v211, s37, v117
	v_perm_b32 v145, v114, v118, s29
	v_dot2c_f32_f16_e32 v224, s35, v145
	v_and_b32_e32 v145, s32, v145
	v_dot2c_f32_f16_e32 v220, s35, v145
	v_perm_b32 v145, v114, v118, s30
	v_dot2c_f32_f16_e32 v225, s35, v145
	v_and_b32_e32 v145, s32, v145
	v_dot2c_f32_f16_e32 v221, s35, v145
	v_perm_b32 v145, v114, v118, s31
	v_dot2c_f32_f16_e32 v222, s35, v145
	v_and_b32_e32 v145, s32, v145
	v_perm_b32 v117, v114, v118, s33
	v_and_b32_e32 v209, s32, v117
	v_dot2c_f32_f16_e32 v223, s35, v117
	v_dot2c_f32_f16_e32 v219, s35, v209
	v_perm_b32 v253, v115, v119, s29
	v_dot2c_f32_f16_e32 v216, s35, v253
	v_and_b32_e32 v253, s32, v253
	v_dot2c_f32_f16_e32 v212, s35, v253
	v_perm_b32 v253, v115, v119, s30
	v_dot2c_f32_f16_e32 v217, s35, v253
	v_and_b32_e32 v253, s32, v253
	v_dot2c_f32_f16_e32 v213, s35, v253
	v_perm_b32 v253, v115, v119, s31
	v_perm_b32 v209, v115, v119, s33
	v_dot2c_f32_f16_e32 v215, s35, v209
	v_and_b32_e32 v209, s32, v209
	v_dot2c_f32_f16_e32 v214, s35, v253
	v_and_b32_e32 v253, s32, v253
	v_dot2c_f32_f16_e32 v211, s35, v209
	v_perm_b32 v117, v68, v72, s29
	v_dot2c_f32_f16_e32 v224, s4, v117
	v_and_b32_e32 v117, s32, v117
	v_dot2c_f32_f16_e32 v220, s4, v117
	v_perm_b32 v117, v68, v72, s30
	v_dot2c_f32_f16_e32 v225, s4, v117
	v_and_b32_e32 v117, s32, v117
	v_dot2c_f32_f16_e32 v221, s4, v117
	v_perm_b32 v117, v68, v72, s31
	v_dot2c_f32_f16_e32 v222, s4, v117
	v_and_b32_e32 v117, s32, v117
	v_perm_b32 v254, v68, v72, s33
	v_and_b32_e32 v254, s32, v254
	v_perm_b32 v209, v68, v72, s33
	v_dot2c_f32_f16_e32 v219, s4, v254
	v_dot2c_f32_f16_e32 v223, s4, v209
	v_perm_b32 v209, v69, v73, s29
	v_dot2c_f32_f16_e32 v216, s4, v209
	v_and_b32_e32 v209, s32, v209
	v_dot2c_f32_f16_e32 v212, s4, v209
	v_perm_b32 v209, v69, v73, s30
	v_dot2c_f32_f16_e32 v217, s4, v209
	v_and_b32_e32 v209, s32, v209
	v_dot2c_f32_f16_e32 v213, s4, v209
	v_perm_b32 v209, v69, v73, s31
	v_perm_b32 v254, v69, v73, s33
	v_dot2c_f32_f16_e32 v215, s4, v254
	s_waitcnt vmcnt(31)
	v_dot8_i32_i4 v68, v248, v62, 0
	v_dot8_i32_i4 v68, v250, v63, v68
	v_dot2c_f32_f16_e32 v210, s39, v149
	v_dot2c_f32_f16_e32 v218, s37, v148
	v_dot2c_f32_f16_e32 v210, s37, v207
	v_lshlrev_b32_e32 v68, 4, v68
	v_dot8_i32_i4 v68, v247, v62, v68
	s_waitcnt vmcnt(30)
	v_dot8_i32_i4 v62, v248, v58, 0
	v_dot8_i32_i4 v62, v250, v59, v62
	v_dot8_i32_i4 v68, v249, v63, v68
	v_dot2c_f32_f16_e32 v218, s35, v145
	v_dot2c_f32_f16_e32 v210, s35, v253
	v_lshlrev_b32_e32 v62, 4, v62
	v_dot8_i32_i4 v62, v247, v58, v62
	s_waitcnt vmcnt(29)
	v_dot8_i32_i4 v58, v248, v54, 0
	v_dot8_i32_i4 v58, v250, v55, v58
	v_dot8_i32_i4 v62, v249, v59, v62
	v_dot2c_f32_f16_e32 v214, s4, v209
	v_and_b32_e32 v209, s32, v209
	v_lshlrev_b32_e32 v58, 4, v58
	v_dot8_i32_i4 v58, v247, v54, v58
	s_waitcnt vmcnt(28)
	v_dot8_i32_i4 v54, v248, v50, 0
	v_dot8_i32_i4 v54, v250, v51, v54
	v_dot8_i32_i4 v58, v249, v55, v58
	v_dot2c_f32_f16_e32 v218, s4, v117
	v_dot2c_f32_f16_e32 v210, s4, v209
	v_lshlrev_b32_e32 v54, 4, v54
	v_dot8_i32_i4 v54, v247, v50, v54
	s_waitcnt vmcnt(27)
	v_dot8_i32_i4 v50, v248, v46, 0
	v_dot8_i32_i4 v50, v250, v47, v50
	v_dot8_i32_i4 v54, v249, v51, v54
	s_add_i32 s24, s25, 2
	s_cmp_lt_u32 s25, 5
	v_lshlrev_b32_e32 v50, 4, v50
	v_dot8_i32_i4 v50, v247, v46, v50
	s_waitcnt vmcnt(26)
	v_dot8_i32_i4 v46, v248, v42, 0
	v_dot8_i32_i4 v46, v250, v43, v46
	v_dot8_i32_i4 v50, v249, v47, v50
	v_cvt_f32_f16_e32 v116, v116
	s_nop 0
	v_lshlrev_b32_e32 v46, 4, v46
	v_dot8_i32_i4 v46, v247, v42, v46
	s_waitcnt vmcnt(25)
	v_dot8_i32_i4 v42, v248, v38, 0
	v_dot8_i32_i4 v42, v250, v39, v42
	v_dot8_i32_i4 v46, v249, v43, v46
	s_nop 1
	v_lshlrev_b32_e32 v42, 4, v42
	v_dot8_i32_i4 v42, v247, v38, v42
	s_waitcnt vmcnt(24)
	v_dot8_i32_i4 v38, v248, v30, 0
	v_dot8_i32_i4 v38, v250, v31, v38
	v_dot8_i32_i4 v42, v249, v39, v42
	s_nop 1
	v_lshlrev_b32_e32 v38, 4, v38
	v_dot8_i32_i4 v38, v247, v30, v38
	v_dot8_i32_i4 v38, v249, v31, v38
	s_waitcnt vmcnt(22)
	v_dot8_i32_i4 v31, v248, v22, 0
	v_dot8_i32_i4 v31, v250, v23, v31
	v_dot8_i32_i4 v30, v248, v34, 0
	v_dot8_i32_i4 v30, v250, v35, v30
	s_nop 0
	v_lshlrev_b32_e32 v31, 4, v31
	v_dot8_i32_i4 v31, v247, v22, v31
	v_dot8_i32_i4 v31, v249, v23, v31
	s_waitcnt vmcnt(20)
	v_dot8_i32_i4 v23, v248, v14, 0
	v_dot8_i32_i4 v23, v250, v15, v23
	v_dot8_i32_i4 v22, v248, v26, 0
	v_dot8_i32_i4 v22, v250, v27, v22
	s_nop 0
	v_lshlrev_b32_e32 v23, 4, v23
	v_dot8_i32_i4 v23, v247, v14, v23
	v_dot8_i32_i4 v23, v249, v15, v23
	s_waitcnt vmcnt(18)
	v_dot8_i32_i4 v15, v248, v6, 0
	v_dot8_i32_i4 v15, v250, v7, v15
	v_dot8_i32_i4 v14, v248, v18, 0
	v_dot8_i32_i4 v14, v250, v19, v14
	s_nop 0
	v_lshlrev_b32_e32 v15, 4, v15
	v_dot8_i32_i4 v15, v247, v6, v15
	v_dot8_i32_i4 v15, v249, v7, v15
	s_waitcnt vmcnt(17)
	v_dot8_i32_i4 v6, v248, v10, 0
	s_waitcnt vmcnt(16)
	v_dot8_i32_i4 v7, v248, v2, 0
	v_dot8_i32_i4 v6, v250, v11, v6
	v_dot8_i32_i4 v7, v250, v3, v7
	v_lshlrev_b32_e32 v30, 4, v30
	v_lshlrev_b32_e32 v22, 4, v22
	v_lshlrev_b32_e32 v14, 4, v14
	v_lshlrev_b32_e32 v6, 4, v6
	v_lshlrev_b32_e32 v7, 4, v7
	v_dot8_i32_i4 v30, v247, v34, v30
	v_dot8_i32_i4 v22, v247, v26, v22
	v_dot8_i32_i4 v14, v247, v18, v14
	v_dot8_i32_i4 v6, v247, v10, v6
	v_dot8_i32_i4 v7, v247, v2, v7
	v_dot8_i32_i4 v30, v249, v35, v30
	v_dot8_i32_i4 v22, v249, v27, v22
	v_dot8_i32_i4 v14, v249, v19, v14
	v_dot8_i32_i4 v6, v249, v11, v6
	v_dot8_i32_i4 v7, v249, v3, v7
	v_permlane32_swap_b32_e32 v68, v30
	v_permlane32_swap_b32_e32 v62, v31
	v_permlane32_swap_b32_e32 v58, v22
	v_permlane32_swap_b32_e32 v54, v23
	v_permlane32_swap_b32_e32 v50, v14
	v_permlane32_swap_b32_e32 v46, v15
	v_permlane32_swap_b32_e32 v42, v6
	v_permlane32_swap_b32_e32 v38, v7
	v_add_u32_e32 v2, v68, v30
	v_add_u32_e32 v3, v62, v31
	v_add_u32_e32 v10, v58, v22
	v_add_u32_e32 v11, v54, v23
	v_add_u32_e32 v14, v50, v14
	v_add_u32_e32 v15, v46, v15
	v_add_u32_e32 v6, v42, v6
	v_add_u32_e32 v7, v38, v7
	v_permlane16_swap_b32_e32 v2, v14
	v_permlane16_swap_b32_e32 v3, v15
	v_permlane16_swap_b32_e32 v10, v6
	v_permlane16_swap_b32_e32 v11, v7
	v_add_u32_e32 v2, v2, v14
	v_add_u32_e32 v3, v3, v15
	v_add_u32_e32 v6, v10, v6
	v_add_u32_e32 v7, v11, v7
	v_cndmask_b32_e64 v10, v6, v2, s[0:1]
	v_cndmask_b32_e64 v2, v2, v6, s[0:1]
	v_cndmask_b32_e64 v6, v7, v3, s[0:1]
	v_cndmask_b32_e64 v3, v3, v7, s[0:1]
	v_add_u32_dpp v2, v2, v10 quad_perm:[2,3,0,1] row_mask:0xf bank_mask:0xf bound_ctrl:1
	ds_bpermute_b32 v7, v66, v71 offset:64
	v_add_u32_dpp v3, v3, v6 quad_perm:[2,3,0,1] row_mask:0xf bank_mask:0xf bound_ctrl:1
	v_cndmask_b32_e64 v6, v3, v2, s[2:3]
	v_cndmask_b32_e64 v2, v2, v3, s[2:3]
	ds_bpermute_b32 v3, v66, v70 offset:64
	v_add_f32_e32 v68, v252, v116
	v_add_u32_dpp v2, v2, v6 quad_perm:[1,0,3,2] row_mask:0xf bank_mask:0xf bound_ctrl:1
	v_and_b32_e32 v6, s32, v254
	v_dot2c_f32_f16_e32 v211, s4, v6
	v_add_u32_dpp v2, v2, v2 row_ror:8 row_mask:0xf bank_mask:0xf bound_ctrl:1
	ds_bpermute_b32 v6, v66, v67 offset:64
	s_nop 0
	v_add_u32_dpp v2, v2, v2 row_ror:4 row_mask:0xf bank_mask:0xf bound_ctrl:1
	v_cvt_f32_i32_e32 v2, v2
	v_add_f32_e32 v2, v251, v2
	v_mul_f32_e32 v2, v244, v2
	s_waitcnt lgkmcnt(1)
	v_mul_f32_e32 v2, v2, v3
	v_fma_f32 v3, |v2|, s28, 1.0
	v_rcp_f32_e32 v3, v3
	v_mul_f32_e32 v11, v2, v2
	v_mul_f32_e32 v11, 0xbf38aa3b, v11
	v_exp_f32_e32 v11, v11
	v_fmamk_f32 v10, v3, 0x3f07dc22, v227
	v_fmaak_f32 v10, v3, v10, 0x3f35f0e3
	v_fmaak_f32 v10, v3, v10, 0xbe11a98e
	v_fmaak_f32 v10, v3, v10, 0x3e027906
	v_mul_f32_e32 v3, v3, v10
	v_mul_f32_e32 v3, v11, v3
	v_mul_f32_e32 v10, v2, v3
	v_fma_f32 v3, -v2, v3, v2
	v_cmp_gt_f32_e64 s[4:5], 0, v2
	s_nop 1
	v_cndmask_b32_e64 v2, v3, v10, s[4:5]
	s_waitcnt lgkmcnt(0)
	v_mul_f32_e32 v2, v2, v6
	v_mul_f32_e32 v2, v2, v7
	v_fma_mixlo_f16 v2, v2, s16, 0
	v_and_b32_e32 v3, 0xffff, v2
	s_cselect_b64 s[4:5], -1, 0
	s_nop 0
	v_mov_b32_dpp v253, v3 quad_perm:[1,0,3,2] row_mask:0xf bank_mask:0xf
	v_lshl_or_b32 v254, v253, 16, v3
	v_cvt_f32_f16_e32 v66, v2
	v_cndmask_b32_e64 v2, v242, v232, s[4:5]
	v_readlane_b32 s5, v254, 0
	v_perm_b32 v14, v60, v64, s29
	s_nop 0
	v_dot2c_f32_f16_e32 v224, s5, v14
	v_and_b32_e32 v14, s32, v14
	v_dot2c_f32_f16_e32 v220, s5, v14
	v_perm_b32 v14, v60, v64, s30
	v_dot2c_f32_f16_e32 v225, s5, v14
	v_and_b32_e32 v14, s32, v14
	v_dot2c_f32_f16_e32 v221, s5, v14
	v_perm_b32 v14, v60, v64, s31
	v_perm_b32 v6, v60, v64, s33
	v_dot2c_f32_f16_e32 v223, s5, v6
	v_and_b32_e32 v6, s32, v6
	v_dot2c_f32_f16_e32 v222, s5, v14
	v_and_b32_e32 v14, s32, v14
	v_dot2c_f32_f16_e32 v219, s5, v6
	v_dot2c_f32_f16_e32 v218, s5, v14
	v_perm_b32 v14, v61, v65, s29
	v_dot2c_f32_f16_e32 v216, s5, v14
	v_and_b32_e32 v14, s32, v14
	v_dot2c_f32_f16_e32 v212, s5, v14
	v_perm_b32 v14, v61, v65, s30
	v_dot2c_f32_f16_e32 v217, s5, v14
	v_and_b32_e32 v14, s32, v14
	v_dot2c_f32_f16_e32 v213, s5, v14
	v_perm_b32 v14, v61, v65, s31
	v_perm_b32 v6, v61, v65, s33
	v_dot2c_f32_f16_e32 v214, s5, v14
	v_and_b32_e32 v14, s32, v14
	v_dot2c_f32_f16_e32 v215, s5, v6
	v_and_b32_e32 v6, s32, v6
	v_cndmask_b32_e32 v2, v2, v231, vcc
	v_dot2c_f32_f16_e32 v210, s5, v14
	v_dot2c_f32_f16_e32 v211, s5, v6
	v_lshlrev_b32_e32 v2, 10, v2
	s_add_i32 s61, s21, 16
	v_readlane_b32 s61, v2, s61
	s_add_i32 s62, s21, 17
	v_readlane_b32 s62, v2, s62
	s_add_i32 s63, s21, 18
	v_readlane_b32 s63, v2, s63
	s_add_i32 s64, s21, 19
	v_readlane_b32 s64, v2, s64
	s_add_i32 s65, s21, 20
	v_readlane_b32 s65, v2, s65
	s_add_i32 s66, s21, 21
	v_readlane_b32 s66, v2, s66
	s_add_i32 s67, s21, 22
	v_readlane_b32 s67, v2, s67
	s_add_i32 s68, s21, 23
	v_readlane_b32 s68, v2, s68
	s_add_i32 s69, s21, 24
	v_readlane_b32 s69, v2, s69
	s_add_i32 s70, s21, 25
	v_readlane_b32 s70, v2, s70
	s_add_i32 s71, s21, 26
	v_readlane_b32 s71, v2, s71
	s_add_i32 s72, s21, 27
	v_readlane_b32 s72, v2, s72
	s_add_i32 s73, s21, 28
	v_readlane_b32 s73, v2, s73
	s_add_i32 s74, s21, 29
	v_readlane_b32 s74, v2, s74
	s_add_i32 s75, s21, 30
	v_readlane_b32 s75, v2, s75
	s_add_i32 s76, s21, 31
	v_readlane_b32 s76, v2, s76
	buffer_load_dwordx4 v[62:65], v194, s[80:83], s61 offen
	buffer_load_dwordx4 v[58:61], v194, s[80:83], s62 offen
	v_readlane_b32 s4, v254, 2
	v_perm_b32 v14, v52, v56, s29
	s_nop 0
	v_dot2c_f32_f16_e32 v224, s4, v14
	v_and_b32_e32 v14, s32, v14
	v_dot2c_f32_f16_e32 v220, s4, v14
	v_perm_b32 v14, v52, v56, s30
	v_dot2c_f32_f16_e32 v225, s4, v14
	v_and_b32_e32 v14, s32, v14
	v_dot2c_f32_f16_e32 v221, s4, v14
	v_perm_b32 v14, v52, v56, s31
	v_perm_b32 v6, v52, v56, s33
	v_dot2c_f32_f16_e32 v223, s4, v6
	v_and_b32_e32 v6, s32, v6
	v_dot2c_f32_f16_e32 v222, s4, v14
	v_and_b32_e32 v14, s32, v14
	v_dot2c_f32_f16_e32 v219, s4, v6
	v_dot2c_f32_f16_e32 v218, s4, v14
	v_perm_b32 v14, v53, v57, s29
	v_dot2c_f32_f16_e32 v216, s4, v14
	v_and_b32_e32 v14, s32, v14
	v_dot2c_f32_f16_e32 v212, s4, v14
	v_perm_b32 v14, v53, v57, s30
	v_dot2c_f32_f16_e32 v217, s4, v14
	v_and_b32_e32 v14, s32, v14
	v_dot2c_f32_f16_e32 v213, s4, v14
	v_perm_b32 v14, v53, v57, s31
	v_perm_b32 v6, v53, v57, s33
	v_dot2c_f32_f16_e32 v214, s4, v14
	v_and_b32_e32 v14, s32, v14
	v_dot2c_f32_f16_e32 v215, s4, v6
	v_and_b32_e32 v6, s32, v6
	v_dot2c_f32_f16_e32 v210, s4, v14
	v_dot2c_f32_f16_e32 v211, s4, v6
	buffer_load_dwordx4 v[54:57], v194, s[80:83], s63 offen
	buffer_load_dwordx4 v[50:53], v194, s[80:83], s64 offen
	v_readlane_b32 s4, v254, 16
	v_perm_b32 v14, v44, v48, s29
	s_nop 0
	v_dot2c_f32_f16_e32 v224, s4, v14
	v_and_b32_e32 v14, s32, v14
	v_dot2c_f32_f16_e32 v220, s4, v14
	v_perm_b32 v14, v44, v48, s30
	v_dot2c_f32_f16_e32 v225, s4, v14
	v_and_b32_e32 v14, s32, v14
	v_dot2c_f32_f16_e32 v221, s4, v14
	v_perm_b32 v14, v44, v48, s31
	v_perm_b32 v6, v44, v48, s33
	v_dot2c_f32_f16_e32 v223, s4, v6
	v_and_b32_e32 v6, s32, v6
	v_dot2c_f32_f16_e32 v222, s4, v14
	v_and_b32_e32 v14, s32, v14
	v_dot2c_f32_f16_e32 v219, s4, v6
	v_dot2c_f32_f16_e32 v218, s4, v14
	v_perm_b32 v14, v45, v49, s29
	v_dot2c_f32_f16_e32 v216, s4, v14
	v_and_b32_e32 v14, s32, v14
	v_dot2c_f32_f16_e32 v212, s4, v14
	v_perm_b32 v14, v45, v49, s30
	v_dot2c_f32_f16_e32 v217, s4, v14
	v_and_b32_e32 v14, s32, v14
	v_dot2c_f32_f16_e32 v213, s4, v14
	v_perm_b32 v14, v45, v49, s31
	v_perm_b32 v6, v45, v49, s33
	v_dot2c_f32_f16_e32 v214, s4, v14
	v_and_b32_e32 v14, s32, v14
	v_dot2c_f32_f16_e32 v215, s4, v6
	v_and_b32_e32 v6, s32, v6
	v_dot2c_f32_f16_e32 v210, s4, v14
	v_dot2c_f32_f16_e32 v211, s4, v6
	buffer_load_dwordx4 v[46:49], v194, s[80:83], s65 offen
	buffer_load_dwordx4 v[42:45], v194, s[80:83], s66 offen
	v_readlane_b32 s4, v254, 18
	v_perm_b32 v14, v32, v40, s29
	s_nop 0
	v_dot2c_f32_f16_e32 v224, s4, v14
	v_and_b32_e32 v14, s32, v14
	v_dot2c_f32_f16_e32 v220, s4, v14
	v_perm_b32 v14, v32, v40, s30
	v_dot2c_f32_f16_e32 v225, s4, v14
	v_and_b32_e32 v14, s32, v14
	v_dot2c_f32_f16_e32 v221, s4, v14
	v_perm_b32 v14, v32, v40, s31
	v_perm_b32 v6, v32, v40, s33
	v_dot2c_f32_f16_e32 v223, s4, v6
	v_and_b32_e32 v6, s32, v6
	v_dot2c_f32_f16_e32 v222, s4, v14
	v_and_b32_e32 v14, s32, v14
	v_dot2c_f32_f16_e32 v219, s4, v6
	v_dot2c_f32_f16_e32 v218, s4, v14
	v_perm_b32 v14, v33, v41, s29
	v_dot2c_f32_f16_e32 v216, s4, v14
	v_and_b32_e32 v14, s32, v14
	v_dot2c_f32_f16_e32 v212, s4, v14
	v_perm_b32 v14, v33, v41, s30
	v_dot2c_f32_f16_e32 v217, s4, v14
	v_and_b32_e32 v14, s32, v14
	v_dot2c_f32_f16_e32 v213, s4, v14
	v_perm_b32 v14, v33, v41, s31
; __device__ __forceinline__ void expert_tokens(const unsigned char* __restrict__ UV, const float* __restrict__ US, const float* __restrict__ VS, ...
;     ...
;         for (int bi = 0; bi < 128 / EB; bi += 2) {
;             EXP_STEP(A, bi);
;             if (bi == 0) { nsu0 = US[ni0]; nsu1 = US[ni1]; nsv0 = VS[ni0]; nsv1 = VS[ni1]; }
;             EXP_STEP(B, bi + 1);
;         }
	v_perm_b32 v6, v33, v41, s33
	v_dot2c_f32_f16_e32 v214, s4, v14
	v_and_b32_e32 v14, s32, v14
	v_dot2c_f32_f16_e32 v215, s4, v6
	v_and_b32_e32 v6, s32, v6
	v_dot2c_f32_f16_e32 v210, s4, v14
	v_dot2c_f32_f16_e32 v211, s4, v6
	buffer_load_dwordx4 v[38:41], v194, s[80:83], s67 offen
	buffer_load_dwordx4 v[30:33], v194, s[80:83], s68 offen
	v_readlane_b32 s4, v254, 32
	v_perm_b32 v14, v24, v36, s29
	s_nop 0
	v_dot2c_f32_f16_e32 v224, s4, v14
	v_and_b32_e32 v14, s32, v14
	v_dot2c_f32_f16_e32 v220, s4, v14
	v_perm_b32 v14, v24, v36, s30
	v_dot2c_f32_f16_e32 v225, s4, v14
	v_and_b32_e32 v14, s32, v14
	v_dot2c_f32_f16_e32 v221, s4, v14
	v_perm_b32 v14, v24, v36, s31
	v_perm_b32 v6, v24, v36, s33
	v_dot2c_f32_f16_e32 v223, s4, v6
	v_and_b32_e32 v6, s32, v6
	v_dot2c_f32_f16_e32 v222, s4, v14
	v_and_b32_e32 v14, s32, v14
	v_dot2c_f32_f16_e32 v219, s4, v6
	v_dot2c_f32_f16_e32 v218, s4, v14
	v_perm_b32 v14, v25, v37, s29
	v_dot2c_f32_f16_e32 v216, s4, v14
	v_and_b32_e32 v14, s32, v14
	v_dot2c_f32_f16_e32 v212, s4, v14
	v_perm_b32 v14, v25, v37, s30
	v_dot2c_f32_f16_e32 v217, s4, v14
	v_and_b32_e32 v14, s32, v14
	v_dot2c_f32_f16_e32 v213, s4, v14
	v_perm_b32 v14, v25, v37, s31
	v_perm_b32 v6, v25, v37, s33
	v_dot2c_f32_f16_e32 v214, s4, v14
	v_and_b32_e32 v14, s32, v14
	v_dot2c_f32_f16_e32 v215, s4, v6
	v_and_b32_e32 v6, s32, v6
	v_dot2c_f32_f16_e32 v210, s4, v14
	v_dot2c_f32_f16_e32 v211, s4, v6
	buffer_load_dwordx4 v[34:37], v194, s[80:83], s69 offen
	buffer_load_dwordx4 v[22:25], v194, s[80:83], s70 offen
	v_readlane_b32 s4, v254, 34
	v_perm_b32 v14, v16, v28, s29
	s_nop 0
	v_dot2c_f32_f16_e32 v224, s4, v14
	v_and_b32_e32 v14, s32, v14
	v_dot2c_f32_f16_e32 v220, s4, v14
	v_perm_b32 v14, v16, v28, s30
	v_dot2c_f32_f16_e32 v225, s4, v14
	v_and_b32_e32 v14, s32, v14
	v_dot2c_f32_f16_e32 v221, s4, v14
	v_perm_b32 v14, v16, v28, s31
	v_perm_b32 v6, v16, v28, s33
	v_dot2c_f32_f16_e32 v223, s4, v6
	v_and_b32_e32 v6, s32, v6
	v_dot2c_f32_f16_e32 v222, s4, v14
	v_and_b32_e32 v14, s32, v14
	v_dot2c_f32_f16_e32 v219, s4, v6
	v_dot2c_f32_f16_e32 v218, s4, v14
	v_perm_b32 v14, v17, v29, s29
	v_dot2c_f32_f16_e32 v216, s4, v14
	v_and_b32_e32 v14, s32, v14
	v_dot2c_f32_f16_e32 v212, s4, v14
	v_perm_b32 v14, v17, v29, s30
	v_dot2c_f32_f16_e32 v217, s4, v14
	v_and_b32_e32 v14, s32, v14
	v_dot2c_f32_f16_e32 v213, s4, v14
	v_perm_b32 v14, v17, v29, s31
	v_perm_b32 v6, v17, v29, s33
	v_dot2c_f32_f16_e32 v214, s4, v14
	v_and_b32_e32 v14, s32, v14
	v_dot2c_f32_f16_e32 v215, s4, v6
	v_and_b32_e32 v6, s32, v6
	v_dot2c_f32_f16_e32 v210, s4, v14
	v_dot2c_f32_f16_e32 v211, s4, v6
	buffer_load_dwordx4 v[26:29], v194, s[80:83], s71 offen
	buffer_load_dwordx4 v[14:17], v194, s[80:83], s72 offen
	v_readlane_b32 s4, v254, 48
	v_perm_b32 v11, v8, v20, s29
	s_nop 0
	v_dot2c_f32_f16_e32 v224, s4, v11
	v_and_b32_e32 v11, s32, v11
	v_dot2c_f32_f16_e32 v220, s4, v11
	v_perm_b32 v11, v8, v20, s30
	v_dot2c_f32_f16_e32 v225, s4, v11
	v_and_b32_e32 v11, s32, v11
	v_dot2c_f32_f16_e32 v221, s4, v11
	v_perm_b32 v11, v8, v20, s31
	v_perm_b32 v6, v8, v20, s33
	v_dot2c_f32_f16_e32 v223, s4, v6
	v_and_b32_e32 v6, s32, v6
	v_dot2c_f32_f16_e32 v222, s4, v11
	v_and_b32_e32 v11, s32, v11
	v_dot2c_f32_f16_e32 v219, s4, v6
	v_perm_b32 v10, v9, v21, s29
	v_dot2c_f32_f16_e32 v216, s4, v10
	v_and_b32_e32 v10, s32, v10
	v_dot2c_f32_f16_e32 v212, s4, v10
	v_perm_b32 v10, v9, v21, s30
	v_dot2c_f32_f16_e32 v217, s4, v10
	v_and_b32_e32 v10, s32, v10
	v_dot2c_f32_f16_e32 v213, s4, v10
	v_perm_b32 v10, v9, v21, s31
	v_perm_b32 v6, v9, v21, s33
	v_dot2c_f32_f16_e32 v214, s4, v10
	v_and_b32_e32 v10, s32, v10
	v_dot2c_f32_f16_e32 v215, s4, v6
	v_and_b32_e32 v6, s32, v6
	v_dot2c_f32_f16_e32 v218, s4, v11
	v_dot2c_f32_f16_e32 v210, s4, v10
	v_dot2c_f32_f16_e32 v211, s4, v6
	buffer_load_dwordx4 v[18:21], v194, s[80:83], s73 offen
	buffer_load_dwordx4 v[6:9], v194, s[80:83], s74 offen
	v_readlane_b32 s4, v254, 50
	v_perm_b32 v254, v4, v12, s29
	s_nop 0
	v_dot2c_f32_f16_e32 v224, s4, v254
	v_and_b32_e32 v254, s32, v254
	v_dot2c_f32_f16_e32 v220, s4, v254
	v_perm_b32 v254, v4, v12, s30
	v_dot2c_f32_f16_e32 v225, s4, v254
	v_and_b32_e32 v254, s32, v254
	v_dot2c_f32_f16_e32 v221, s4, v254
	v_perm_b32 v254, v4, v12, s31
	v_perm_b32 v3, v4, v12, s33
	v_dot2c_f32_f16_e32 v223, s4, v3
	v_and_b32_e32 v3, s32, v3
	v_dot2c_f32_f16_e32 v222, s4, v254
	v_and_b32_e32 v254, s32, v254
	v_dot2c_f32_f16_e32 v219, s4, v3
	v_perm_b32 v11, v5, v13, s29
	v_dot2c_f32_f16_e32 v216, s4, v11
	v_and_b32_e32 v11, s32, v11
	v_dot2c_f32_f16_e32 v212, s4, v11
	v_perm_b32 v11, v5, v13, s30
	v_dot2c_f32_f16_e32 v217, s4, v11
	v_and_b32_e32 v11, s32, v11
	v_dot2c_f32_f16_e32 v213, s4, v11
	v_perm_b32 v11, v5, v13, s31
	v_perm_b32 v3, v5, v13, s33
	v_dot2c_f32_f16_e32 v214, s4, v11
	v_and_b32_e32 v11, s32, v11
	v_dot2c_f32_f16_e32 v215, s4, v3
	v_and_b32_e32 v3, s32, v3
	v_dot2c_f32_f16_e32 v218, s4, v254
	v_dot2c_f32_f16_e32 v210, s4, v11
	v_dot2c_f32_f16_e32 v211, s4, v3
	buffer_load_dwordx4 v[10:13], v194, s[80:83], s75 offen
	buffer_load_dwordx4 v[2:5], v194, s[80:83], s76 offen
	v_add_f32_e32 v252, v68, v66
	s_add_i32 s21, s21, 32
	s_and_b64 vcc, exec, s[22:23]
	s_cbranch_vccnz .LBB0_1013
	s_waitcnt vmcnt(23)
	v_mov_b64_e32 v[158:159], v[112:113]
	v_mov_b64_e32 v[190:191], v[80:81]
	v_mov_b64_e32 v[186:187], v[76:77]
	v_mov_b64_e32 v[182:183], v[88:89]
	v_mov_b64_e32 v[178:179], v[84:85]
	v_mov_b64_e32 v[174:175], v[96:97]
	v_mov_b64_e32 v[170:171], v[92:93]
	v_mov_b64_e32 v[166:167], v[104:105]
	v_mov_b64_e32 v[162:163], v[100:101]
	v_mov_b64_e32 v[156:157], v[110:111]
	s_waitcnt vmcnt(22)
	v_mov_b64_e32 v[154:155], v[108:109]
	s_waitcnt vmcnt(21)
	v_mov_b64_e32 v[150:151], v[126:127]
	s_waitcnt vmcnt(20)
	v_mov_b64_e32 v[146:147], v[122:123]
	s_waitcnt vmcnt(19)
	v_mov_b64_e32 v[116:117], v[132:133]
	s_waitcnt vmcnt(18)
	v_mov_b64_e32 v[112:113], v[128:129]
	s_waitcnt vmcnt(17)
	v_mov_b64_e32 v[70:71], v[140:141]
	s_waitcnt vmcnt(16)
	v_mov_b64_e32 v[66:67], v[136:137]
	v_mov_b64_e32 v[188:189], v[78:79]
	v_mov_b64_e32 v[184:185], v[74:75]
	v_mov_b64_e32 v[180:181], v[86:87]
	v_mov_b64_e32 v[176:177], v[82:83]
	v_mov_b64_e32 v[172:173], v[94:95]
	v_mov_b64_e32 v[168:169], v[90:91]
	v_mov_b64_e32 v[164:165], v[102:103]
	v_mov_b64_e32 v[160:161], v[98:99]
	v_mov_b64_e32 v[152:153], v[106:107]
	v_mov_b64_e32 v[148:149], v[124:125]
	v_mov_b64_e32 v[144:145], v[120:121]
	v_mov_b64_e32 v[118:119], v[134:135]
	v_mov_b64_e32 v[114:115], v[130:131]
	v_mov_b64_e32 v[72:73], v[142:143]
	v_mov_b64_e32 v[68:69], v[138:139]
	s_mov_b32 s25, s24
	s_branch .LBB0_1019
